# speedup vs baseline: 1.0496x; 1.0196x over previous
_Z11prep_kernel8PrepArgsPc:
	s_load_dword s3, s[0:1], 0x104
	s_load_dwordx2 s[4:5], s[0:1], 0xf0
	s_mov_b32 s6, 0xffff
	s_waitcnt lgkmcnt(0)
	s_and_b32 s7, s3, 0xffff
	s_mul_i32 s7, s2, s7
	v_add_u32_e32 v2, s7, v0
	v_cmp_lt_i32_e32 vcc, s6, v2
	s_and_saveexec_b64 s[6:7], vcc
	s_xor_b64 s[6:7], exec, s[6:7]
	s_cbranch_execz .LBB0_48
	s_mov_b32 s8, 0x1ffff
	v_cmp_lt_u32_e32 vcc, s8, v2
	s_and_saveexec_b64 s[8:9], vcc
	s_xor_b64 s[8:9], exec, s[8:9]
	s_cbranch_execz .LBB0_44
	s_mov_b32 s10, 0x27fff
	v_cmp_lt_u32_e32 vcc, s10, v2
	s_and_saveexec_b64 s[10:11], vcc
	s_xor_b64 s[10:11], exec, s[10:11]
	s_cbranch_execz .LBB0_41
	s_mov_b32 s12, 0x2ffff
	v_cmp_lt_u32_e32 vcc, s12, v2
	s_and_saveexec_b64 s[12:13], vcc
	s_xor_b64 s[12:13], exec, s[12:13]
	s_cbranch_execz .LBB0_38
	s_mov_b32 s14, 0x31fff
	v_cmp_lt_u32_e32 vcc, s14, v2
	s_and_saveexec_b64 s[14:15], vcc
	s_xor_b64 s[14:15], exec, s[14:15]
	s_cbranch_execz .LBB0_35
	s_mov_b32 s16, 0x327ff
	v_cmp_lt_u32_e32 vcc, s16, v2
	s_and_saveexec_b64 s[16:17], vcc
	s_xor_b64 s[16:17], exec, s[16:17]
	s_cbranch_execz .LBB0_28
	s_mov_b32 s18, 0x32bff
	v_cmp_lt_u32_e32 vcc, s18, v2
	s_and_saveexec_b64 s[18:19], vcc
	s_xor_b64 s[18:19], exec, s[18:19]
	s_cbranch_execz .LBB0_23
	s_mov_b32 s20, 0x333ff
	v_cmp_lt_u32_e32 vcc, s20, v2
	s_and_saveexec_b64 s[20:21], vcc
	s_xor_b64 s[20:21], exec, s[20:21]
	s_cbranch_execz .LBB0_20
	s_mov_b32 s22, 0x334ff
	v_cmp_lt_u32_e32 vcc, s22, v2
	s_and_saveexec_b64 s[22:23], vcc
	s_xor_b64 s[22:23], exec, s[22:23]
	s_cbranch_execz .LBB0_15
	s_mov_b32 s24, 0x3b500
	v_cmp_gt_u32_e32 vcc, s24, v2
	s_and_saveexec_b64 s[24:25], vcc
	s_cbranch_execz .LBB0_14
	s_load_dwordx8 s[36:43], s[0:1], 0xc0
	s_load_dwordx4 s[28:31], s[0:1], 0xe0
	v_add_u32_e32 v8, 0xfffccb00, v2
	s_movk_i32 s26, 0x4000
	v_and_b32_e32 v10, 63, v2
	v_mov_b32_e32 v1, 0x80
	v_mov_b32_e32 v2, 0x100
	v_cmp_gt_u32_e32 vcc, s26, v8
	s_waitcnt lgkmcnt(0)
	v_mov_b32_e32 v3, s41
	s_mul_i32 s2, s2, s3
	v_cndmask_b32_e32 v11, v1, v2, vcc
	v_mov_b32_e32 v1, s39
	v_mov_b32_e32 v2, s37
	v_cndmask_b32_e32 v5, v1, v2, vcc
	v_mov_b32_e32 v1, s38
	v_mov_b32_e32 v2, s36
	v_cndmask_b32_e32 v4, v1, v2, vcc
	v_mov_b32_e32 v2, s29
	v_cndmask_b32_e32 v7, v2, v3, vcc
	v_mov_b32_e32 v2, s28
	v_mov_b32_e32 v3, s40
	v_cndmask_b32_e32 v6, v2, v3, vcc
	v_mov_b32_e32 v2, s31
	v_mov_b32_e32 v3, s43
	v_bfe_u32 v9, v8, 6, 8
	v_cndmask_b32_e64 v1, 7, 8, vcc
	v_cndmask_b32_e32 v13, v2, v3, vcc
	v_mov_b32_e32 v2, s30
	v_mov_b32_e32 v3, s42
	v_add_u16_e32 v0, s2, v0
	v_lshlrev_b32_e32 v1, v1, v9
	v_cndmask_b32_e32 v12, v2, v3, vcc
	v_mov_b32_e32 v3, 0
	v_and_b32_e32 v0, 63, v0
	v_lshlrev_b32_e32 v2, 2, v1
	v_lshlrev_b32_e32 v14, 2, v0
	v_mov_b32_e32 v15, v3
	v_lshl_add_u64 v[0:1], v[2:3], 0, v[14:15]
	v_lshl_add_u64 v[0:1], v[4:5], 0, v[0:1]
	v_lshl_add_u64 v[4:5], v[6:7], 0, v[14:15]
	v_lshl_add_u64 v[6:7], v[12:13], 0, v[14:15]
	s_mov_b64 s[2:3], 0
	s_mov_b64 s[26:27], 0x100
	v_mov_b32_e32 v12, v10
	v_mov_b32_e32 v2, v3
	global_load_dword v14, v[0:1], off
	global_load_dword v16, v[4:5], off
	global_load_dword v17, v[6:7], off
	global_load_dword v18, v[0:1], off offset:256
	global_load_dword v20, v[4:5], off offset:256
	global_load_dword v21, v[6:7], off offset:256
	v_cmp_lt_u32_e32 vcc, 0x80, v11
	s_and_saveexec_b64 s[2:3], vcc
	global_load_dword v22, v[0:1], off offset:512
	global_load_dword v24, v[4:5], off offset:512
	global_load_dword v25, v[6:7], off offset:512
	global_load_dword v26, v[0:1], off offset:768
	global_load_dword v28, v[4:5], off offset:768
	global_load_dword v29, v[6:7], off offset:768
	s_mov_b64 exec, s[2:3]
	s_waitcnt vmcnt(0)
	v_pk_fma_f32 v[2:3], v[14:15], v[16:17], v[2:3] op_sel_hi:[0,1,1]
	v_pk_fma_f32 v[2:3], v[18:19], v[20:21], v[2:3] op_sel_hi:[0,1,1]
	s_and_saveexec_b64 s[2:3], vcc
	v_pk_fma_f32 v[2:3], v[22:23], v[24:25], v[2:3] op_sel_hi:[0,1,1]
	v_pk_fma_f32 v[2:3], v[26:27], v[28:29], v[2:3] op_sel_hi:[0,1,1]
	s_mov_b64 exec, s[2:3]
	s_or_b64 exec, exec, s[2:3]
	v_mbcnt_lo_u32_b32 v0, -1, 0
	v_mbcnt_hi_u32_b32 v4, -1, v0
	v_and_b32_e32 v0, 64, v4
	v_add_u32_e32 v5, 64, v0
	v_xor_b32_e32 v0, 32, v4
	v_cmp_lt_i32_e32 vcc, v0, v5
	s_nop 1
	v_cndmask_b32_e32 v0, v4, v0, vcc
	v_lshlrev_b32_e32 v0, 2, v0
	ds_bpermute_b32 v1, v0, v2
	ds_bpermute_b32 v0, v0, v3
	s_waitcnt lgkmcnt(1)
	v_add_f32_e32 v1, v2, v1
	v_xor_b32_e32 v2, 16, v4
	v_cmp_lt_i32_e32 vcc, v2, v5
	s_waitcnt lgkmcnt(0)
	v_add_f32_e32 v0, v3, v0
	v_cndmask_b32_e32 v2, v4, v2, vcc
	v_lshlrev_b32_e32 v2, 2, v2
	ds_bpermute_b32 v3, v2, v1
	ds_bpermute_b32 v2, v2, v0
	s_waitcnt lgkmcnt(1)
	v_add_f32_e32 v1, v1, v3
	s_waitcnt lgkmcnt(0)
	v_add_f32_e32 v0, v0, v2
	v_xor_b32_e32 v2, 8, v4
	v_cmp_lt_i32_e32 vcc, v2, v5
	s_nop 1
	v_cndmask_b32_e32 v2, v4, v2, vcc
	v_lshlrev_b32_e32 v2, 2, v2
	ds_bpermute_b32 v3, v2, v1
	ds_bpermute_b32 v2, v2, v0
	s_waitcnt lgkmcnt(1)
	v_add_f32_e32 v1, v1, v3
	s_waitcnt lgkmcnt(0)
	v_add_f32_e32 v0, v0, v2
	v_xor_b32_e32 v2, 4, v4
	v_cmp_lt_i32_e32 vcc, v2, v5
	s_nop 1
	v_cndmask_b32_e32 v2, v4, v2, vcc
	v_lshlrev_b32_e32 v2, 2, v2
	ds_bpermute_b32 v3, v2, v1
	ds_bpermute_b32 v2, v2, v0
	s_waitcnt lgkmcnt(1)
	v_add_f32_e32 v1, v1, v3
	s_waitcnt lgkmcnt(0)
	v_add_f32_e32 v2, v0, v2
	v_xor_b32_e32 v0, 2, v4
	v_cmp_lt_i32_e32 vcc, v0, v5
	s_nop 1
	v_cndmask_b32_e32 v0, v4, v0, vcc
	v_lshlrev_b32_e32 v0, 2, v0
	ds_bpermute_b32 v3, v0, v1
	ds_bpermute_b32 v6, v0, v2
	s_waitcnt lgkmcnt(1)
	v_add_f32_e32 v0, v1, v3
	s_waitcnt lgkmcnt(0)
	v_add_f32_e32 v1, v2, v6
	v_xor_b32_e32 v2, 1, v4
	v_cmp_lt_i32_e32 vcc, v2, v5
	s_nop 1
	v_cndmask_b32_e32 v2, v4, v2, vcc
	v_lshlrev_b32_e32 v3, 2, v2
	ds_bpermute_b32 v2, v3, v0
	ds_bpermute_b32 v3, v3, v1
	v_cmp_eq_u32_e32 vcc, 0, v10
	s_and_b64 exec, exec, vcc
	s_cbranch_execz .LBB0_14
	s_waitcnt lgkmcnt(1)
	v_add_f32_e32 v5, v0, v2
	v_lshrrev_b32_e32 v0, 5, v8
	s_mov_b32 s2, 0x7fffe00
	v_and_or_b32 v0, v0, s2, v9
	s_waitcnt lgkmcnt(0)
	v_add_f32_e32 v4, v1, v3
	v_lshlrev_b32_e32 v0, 2, v0
	v_mov_b32_e32 v1, 0
	v_lshl_add_u64 v[0:1], s[4:5], 0, v[0:1]
	s_mov_b64 s[2:3], 0x209200
	v_lshl_add_u64 v[2:3], v[0:1], 0, s[2:3]
	v_add_co_u32_e32 v0, vcc, 0x209000, v0
	s_nop 1
	v_addc_co_u32_e32 v1, vcc, 0, v1, vcc
	global_store_dword v[0:1], v5, off offset:512
	global_store_dword v[2:3], v4, off offset:1024

	.amdhsa_kernel _Z11prep_kernel8PrepArgsPc
		.amdhsa_group_segment_fixed_size 0
		.amdhsa_private_segment_fixed_size 0
		.amdhsa_kernarg_size 504
		.amdhsa_user_sgpr_count 2
		.amdhsa_user_sgpr_dispatch_ptr 0
		.amdhsa_user_sgpr_queue_ptr 0
		.amdhsa_user_sgpr_kernarg_segment_ptr 1
		.amdhsa_user_sgpr_dispatch_id 0
		.amdhsa_user_sgpr_kernarg_preload_length 0
		.amdhsa_user_sgpr_kernarg_preload_offset 0
		.amdhsa_user_sgpr_private_segment_size 0
		.amdhsa_uses_dynamic_stack 0
		.amdhsa_enable_private_segment 0
		.amdhsa_system_sgpr_workgroup_id_x 1
		.amdhsa_system_sgpr_workgroup_id_y 0
		.amdhsa_system_sgpr_workgroup_id_z 0
		.amdhsa_system_sgpr_workgroup_info 0
		.amdhsa_system_vgpr_workitem_id 0
		.amdhsa_next_free_vgpr 30
		.amdhsa_next_free_sgpr 44
		.amdhsa_accum_offset 32
		.amdhsa_reserve_vcc 1
		.amdhsa_float_round_mode_32 0
		.amdhsa_float_round_mode_16_64 0
		.amdhsa_float_denorm_mode_32 3
		.amdhsa_float_denorm_mode_16_64 3
		.amdhsa_dx10_clamp 1
		.amdhsa_ieee_mode 1
		.amdhsa_fp16_overflow 0
		.amdhsa_tg_split 0
		.amdhsa_exception_fp_ieee_invalid_op 0
		.amdhsa_exception_fp_denorm_src 0
		.amdhsa_exception_fp_ieee_div_zero 0
		.amdhsa_exception_fp_ieee_overflow 0
		.amdhsa_exception_fp_ieee_underflow 0
		.amdhsa_exception_fp_ieee_inexact 0
		.amdhsa_exception_int_div_zero 0
	.end_amdhsa_kernel

_Z12gat3s_kernelPKfPKDF16_S0_Pf:
	s_load_dwordx4 s[4:7], s[0:1], 0x0
	s_load_dwordx4 s[8:11], s[0:1], 0x10
	v_lshlrev_b32_e32 v1, 4, v0
	v_and_b32_e32 v2, 31, v0
	v_and_b32_e32 v3, 32, v0
	s_lshl_b32 s3, s2, 3
	s_andn2_b32 s3, s3, 31
	s_and_b32 s12, s2, 3
	s_lshl_b32 s13, s12, 14
	s_lshl_b32 s12, s12, 5
	v_add_u32_e32 v8, s3, v2
	v_lshlrev_b32_e32 v8, 2, v8
	v_add_u32_e32 v10, s12, v2
	v_lshlrev_b32_e32 v10, 2, v10
	v_lshlrev_b32_e32 v11, 2, v0
	v_add_u32_e32 v12, 0x1000, v1
	v_add_u32_e32 v13, 0x2000, v1
	v_add_u32_e32 v14, 0x3000, v1
	s_mov_b32 s16, 0x3fb8aa3b
	s_mov_b32 s17, 0x3e4ccccd
	s_waitcnt lgkmcnt(0)
	global_load_dwordx4 v[4:7], v1, s[4:5]
	global_load_dword v8, v8, s[4:5] offset:1024
	global_load_dword v9, v10, s[8:9]
	s_add_u32 s14, s6, s13
	s_addc_u32 s15, s7, 0
	global_load_dwordx4 v[16:19], v1, s[14:15]
	global_load_dwordx4 v[20:23], v1, s[14:15] offset:1024
	global_load_dwordx4 v[24:27], v1, s[14:15] offset:2048
	global_load_dwordx4 v[28:31], v1, s[14:15] offset:3072
	global_load_dwordx4 v[32:35], v12, s[14:15]
	global_load_dwordx4 v[36:39], v12, s[14:15] offset:1024
	global_load_dwordx4 v[40:43], v12, s[14:15] offset:2048
	global_load_dwordx4 v[44:47], v12, s[14:15] offset:3072
	global_load_dwordx4 v[48:51], v13, s[14:15]
	global_load_dwordx4 v[52:55], v13, s[14:15] offset:1024
	global_load_dwordx4 v[56:59], v13, s[14:15] offset:2048
	global_load_dwordx4 v[60:63], v13, s[14:15] offset:3072
	global_load_dwordx4 v[64:67], v14, s[14:15]
	global_load_dwordx4 v[68:71], v14, s[14:15] offset:1024
	global_load_dwordx4 v[72:75], v14, s[14:15] offset:2048
	global_load_dwordx4 v[76:79], v14, s[14:15] offset:3072
	s_waitcnt vmcnt(18)
	v_max_f32_e32 v80, v4, v5
	v_max3_f32 v80, v80, v6, v7
	ds_write_b32 v11, v80
	v_mov_b32_e32 v82, 0
	s_waitcnt lgkmcnt(0)
	ds_read_b128 v[96:99], v82
	ds_read_b128 v[100:103], v82 offset:16
	ds_read_b128 v[104:107], v82 offset:32
	ds_read_b128 v[108:111], v82 offset:48
	ds_read_b128 v[112:115], v82 offset:64
	ds_read_b128 v[116:119], v82 offset:80
	ds_read_b128 v[120:123], v82 offset:96
	ds_read_b128 v[124:127], v82 offset:112
	s_waitcnt lgkmcnt(0)
	ds_read_b128 v[128:131], v82 offset:128
	ds_read_b128 v[132:135], v82 offset:144
	ds_read_b128 v[136:139], v82 offset:160
	ds_read_b128 v[140:143], v82 offset:176
	ds_read_b128 v[144:147], v82 offset:192
	ds_read_b128 v[148:151], v82 offset:208
	ds_read_b128 v[152:155], v82 offset:224
	ds_read_b128 v[156:159], v82 offset:240
	v_max3_f32 v81, v96, v97, v98
	v_max3_f32 v81, v81, v99, v100
	v_max3_f32 v81, v81, v101, v102
	v_max3_f32 v81, v81, v103, v104
	v_max3_f32 v81, v81, v105, v106
	v_max3_f32 v81, v81, v107, v108
	v_max3_f32 v81, v81, v109, v110
	v_max3_f32 v81, v81, v111, v112
	v_max3_f32 v81, v81, v113, v114
	v_max3_f32 v81, v81, v115, v116
	v_max3_f32 v81, v81, v117, v118
	v_max3_f32 v81, v81, v119, v120
	v_max3_f32 v81, v81, v121, v122
	v_max3_f32 v81, v81, v123, v124
	v_max3_f32 v81, v81, v125, v126
	v_max_f32_e32 v81, v81, v127
	s_waitcnt lgkmcnt(0)
	v_max3_f32 v81, v81, v128, v129
	v_max3_f32 v81, v81, v130, v131
	v_max3_f32 v81, v81, v132, v133
	v_max3_f32 v81, v81, v134, v135
	v_max3_f32 v81, v81, v136, v137
	v_max3_f32 v81, v81, v138, v139
	v_max3_f32 v81, v81, v140, v141
	v_max3_f32 v81, v81, v142, v143
	v_max3_f32 v81, v81, v144, v145
	v_max3_f32 v81, v81, v146, v147
	v_max3_f32 v81, v81, v148, v149
	v_max3_f32 v81, v81, v150, v151
	v_max3_f32 v81, v81, v152, v153
	v_max3_f32 v81, v81, v154, v155
	v_max3_f32 v81, v81, v156, v157
	v_max3_f32 v81, v81, v158, v159
	v_sub_f32_e32 v88, v4, v81
	v_sub_f32_e32 v89, v5, v81
	v_sub_f32_e32 v90, v6, v81
	v_sub_f32_e32 v91, v7, v81
	v_mul_f32_e32 v92, s17, v88
	v_mul_f32_e32 v93, s17, v89
	v_mul_f32_e32 v94, s17, v90
	v_mul_f32_e32 v95, s17, v91
	v_mul_f32_e32 v88, s16, v88
	v_mul_f32_e32 v89, s16, v89
	v_mul_f32_e32 v90, s16, v90
	v_mul_f32_e32 v91, s16, v91
	v_mul_f32_e32 v92, s16, v92
	v_mul_f32_e32 v93, s16, v93
	v_mul_f32_e32 v94, s16, v94
	v_mul_f32_e32 v95, s16, v95
	v_exp_f32_e32 v88, v88
	v_exp_f32_e32 v89, v89
	v_exp_f32_e32 v90, v90
	v_exp_f32_e32 v91, v91
	v_exp_f32_e32 v92, v92
	v_exp_f32_e32 v93, v93
	v_exp_f32_e32 v94, v94
	v_exp_f32_e32 v95, v95
	s_waitcnt vmcnt(17)
	v_add_f32_e32 v82, v81, v8
	v_mul_f32_e32 v83, s17, v82
	v_max_f32_e32 v86, v82, v83
	v_sub_f32_e32 v84, v82, v86
	v_sub_f32_e32 v87, v83, v86
	ds_write_b128 v1, v[88:91]
	ds_write_b128 v1, v[92:95] offset:1024
	v_mul_f32_e32 v84, s16, v84
	v_mul_f32_e32 v87, s16, v87
	v_exp_f32_e32 v84, v84
	v_exp_f32_e32 v86, v87
	s_nop 0
	v_mov_b32_e32 v85, v84
	v_mov_b32_e32 v87, v86
	s_waitcnt lgkmcnt(0)
	v_mov_b32_e32 v152, 0x3c003c00
	v_mov_b32_e32 v153, 0x3c003c00
	v_mov_b32_e32 v154, 0x3c003c00
	v_mov_b32_e32 v155, 0x3c003c00
	ds_read_b128 v[96:99], v3
	ds_read_b128 v[100:103], v3 offset:16
	ds_read_b128 v[104:107], v3 offset:1024
	ds_read_b128 v[108:111], v3 offset:1040
	ds_read_b128 v[112:115], v3 offset:64
	ds_read_b128 v[116:119], v3 offset:80
	ds_read_b128 v[120:123], v3 offset:1088
	ds_read_b128 v[124:127], v3 offset:1104
	s_waitcnt lgkmcnt(4)
	v_pk_mul_f32 v[128:129], v[96:97], v[84:85]
	v_pk_mul_f32 v[136:137], v[104:105], v[86:87]
	v_pk_mul_f32 v[130:131], v[98:99], v[84:85]
	v_pk_mul_f32 v[138:139], v[106:107], v[86:87]
	v_pk_mul_f32 v[132:133], v[100:101], v[84:85]
	v_pk_mul_f32 v[140:141], v[108:109], v[86:87]
	v_pk_mul_f32 v[134:135], v[102:103], v[84:85]
	v_pk_mul_f32 v[142:143], v[110:111], v[86:87]
	v_max_f32_e32 v128, v128, v136
	v_max_f32_e32 v129, v129, v137
	v_max_f32_e32 v130, v130, v138
	v_max_f32_e32 v131, v131, v139
	v_max_f32_e32 v132, v132, v140
	v_max_f32_e32 v133, v133, v141
	v_max_f32_e32 v134, v134, v142
	v_max_f32_e32 v135, v135, v143
	v_cvt_pk_f16_f32 v144, v128, v129
	v_cvt_pk_f16_f32 v145, v130, v131
	v_cvt_pk_f16_f32 v146, v132, v133
	v_cvt_pk_f16_f32 v147, v134, v135
	s_waitcnt vmcnt(15)
	s_nop 0
	v_mfma_f32_32x32x16_f16 v[160:175], v[144:147], v[16:19], 0
	v_mfma_f32_32x32x16_f16 v[176:191], v[152:155], v[144:147], 0
	ds_read_b128 v[96:99], v3 offset:128
	ds_read_b128 v[100:103], v3 offset:144
	ds_read_b128 v[104:107], v3 offset:1152
	ds_read_b128 v[108:111], v3 offset:1168
	s_waitcnt lgkmcnt(4)
	v_pk_mul_f32 v[128:129], v[112:113], v[84:85]
	v_pk_mul_f32 v[136:137], v[120:121], v[86:87]
	v_pk_mul_f32 v[130:131], v[114:115], v[84:85]
	v_pk_mul_f32 v[138:139], v[122:123], v[86:87]
	v_pk_mul_f32 v[132:133], v[116:117], v[84:85]
	v_pk_mul_f32 v[140:141], v[124:125], v[86:87]
	v_pk_mul_f32 v[134:135], v[118:119], v[84:85]
	v_pk_mul_f32 v[142:143], v[126:127], v[86:87]
	v_max_f32_e32 v128, v128, v136
	v_max_f32_e32 v129, v129, v137
	v_max_f32_e32 v130, v130, v138
	v_max_f32_e32 v131, v131, v139
	v_max_f32_e32 v132, v132, v140
	v_max_f32_e32 v133, v133, v141
	v_max_f32_e32 v134, v134, v142
	v_max_f32_e32 v135, v135, v143
	v_cvt_pk_f16_f32 v148, v128, v129
	v_cvt_pk_f16_f32 v149, v130, v131
	v_cvt_pk_f16_f32 v150, v132, v133
	v_cvt_pk_f16_f32 v151, v134, v135
	s_waitcnt vmcnt(14)
	s_nop 0
	v_mfma_f32_32x32x16_f16 v[160:175], v[148:151], v[20:23], v[160:175]
	v_mfma_f32_32x32x16_f16 v[176:191], v[152:155], v[148:151], v[176:191]
	ds_read_b128 v[112:115], v3 offset:192
	ds_read_b128 v[116:119], v3 offset:208
	ds_read_b128 v[120:123], v3 offset:1216
	ds_read_b128 v[124:127], v3 offset:1232
	s_waitcnt lgkmcnt(4)
	v_pk_mul_f32 v[128:129], v[96:97], v[84:85]
	v_pk_mul_f32 v[136:137], v[104:105], v[86:87]
	v_pk_mul_f32 v[130:131], v[98:99], v[84:85]
	v_pk_mul_f32 v[138:139], v[106:107], v[86:87]
	v_pk_mul_f32 v[132:133], v[100:101], v[84:85]
	v_pk_mul_f32 v[140:141], v[108:109], v[86:87]
	v_pk_mul_f32 v[134:135], v[102:103], v[84:85]
	v_pk_mul_f32 v[142:143], v[110:111], v[86:87]
	v_max_f32_e32 v128, v128, v136
	v_max_f32_e32 v129, v129, v137
	v_max_f32_e32 v130, v130, v138
	v_max_f32_e32 v131, v131, v139
	v_max_f32_e32 v132, v132, v140
	v_max_f32_e32 v133, v133, v141
	v_max_f32_e32 v134, v134, v142
	v_max_f32_e32 v135, v135, v143
	v_cvt_pk_f16_f32 v144, v128, v129
	v_cvt_pk_f16_f32 v145, v130, v131
	v_cvt_pk_f16_f32 v146, v132, v133
	v_cvt_pk_f16_f32 v147, v134, v135
	s_waitcnt vmcnt(13)
	s_nop 0
	v_mfma_f32_32x32x16_f16 v[160:175], v[144:147], v[24:27], v[160:175]
	v_mfma_f32_32x32x16_f16 v[176:191], v[152:155], v[144:147], v[176:191]
	ds_read_b128 v[96:99], v3 offset:256
	ds_read_b128 v[100:103], v3 offset:272
	ds_read_b128 v[104:107], v3 offset:1280
	ds_read_b128 v[108:111], v3 offset:1296
	s_waitcnt lgkmcnt(4)
	v_pk_mul_f32 v[128:129], v[112:113], v[84:85]
	v_pk_mul_f32 v[136:137], v[120:121], v[86:87]
	v_pk_mul_f32 v[130:131], v[114:115], v[84:85]
	v_pk_mul_f32 v[138:139], v[122:123], v[86:87]
	v_pk_mul_f32 v[132:133], v[116:117], v[84:85]
	v_pk_mul_f32 v[140:141], v[124:125], v[86:87]
	v_pk_mul_f32 v[134:135], v[118:119], v[84:85]
	v_pk_mul_f32 v[142:143], v[126:127], v[86:87]
	v_max_f32_e32 v128, v128, v136
	v_max_f32_e32 v129, v129, v137
	v_max_f32_e32 v130, v130, v138
	v_max_f32_e32 v131, v131, v139
	v_max_f32_e32 v132, v132, v140
	v_max_f32_e32 v133, v133, v141
	v_max_f32_e32 v134, v134, v142
	v_max_f32_e32 v135, v135, v143
	v_cvt_pk_f16_f32 v148, v128, v129
	v_cvt_pk_f16_f32 v149, v130, v131
	v_cvt_pk_f16_f32 v150, v132, v133
	v_cvt_pk_f16_f32 v151, v134, v135
	s_waitcnt vmcnt(12)
	s_nop 0
	v_mfma_f32_32x32x16_f16 v[160:175], v[148:151], v[28:31], v[160:175]
	v_mfma_f32_32x32x16_f16 v[176:191], v[152:155], v[148:151], v[176:191]
	ds_read_b128 v[112:115], v3 offset:320
	ds_read_b128 v[116:119], v3 offset:336
	ds_read_b128 v[120:123], v3 offset:1344
	ds_read_b128 v[124:127], v3 offset:1360
	s_waitcnt lgkmcnt(4)
	v_pk_mul_f32 v[128:129], v[96:97], v[84:85]
	v_pk_mul_f32 v[136:137], v[104:105], v[86:87]
	v_pk_mul_f32 v[130:131], v[98:99], v[84:85]
	v_pk_mul_f32 v[138:139], v[106:107], v[86:87]
	v_pk_mul_f32 v[132:133], v[100:101], v[84:85]
	v_pk_mul_f32 v[140:141], v[108:109], v[86:87]
	v_pk_mul_f32 v[134:135], v[102:103], v[84:85]
	v_pk_mul_f32 v[142:143], v[110:111], v[86:87]
	v_max_f32_e32 v128, v128, v136
	v_max_f32_e32 v129, v129, v137
	v_max_f32_e32 v130, v130, v138
	v_max_f32_e32 v131, v131, v139
	v_max_f32_e32 v132, v132, v140
	v_max_f32_e32 v133, v133, v141
	v_max_f32_e32 v134, v134, v142
	v_max_f32_e32 v135, v135, v143
	v_cvt_pk_f16_f32 v144, v128, v129
	v_cvt_pk_f16_f32 v145, v130, v131
	v_cvt_pk_f16_f32 v146, v132, v133
	v_cvt_pk_f16_f32 v147, v134, v135
	s_waitcnt vmcnt(11)
	s_nop 0
	v_mfma_f32_32x32x16_f16 v[160:175], v[144:147], v[32:35], v[160:175]
	v_mfma_f32_32x32x16_f16 v[176:191], v[152:155], v[144:147], v[176:191]
	ds_read_b128 v[96:99], v3 offset:384
	ds_read_b128 v[100:103], v3 offset:400
	ds_read_b128 v[104:107], v3 offset:1408
	ds_read_b128 v[108:111], v3 offset:1424
	s_waitcnt lgkmcnt(4)
	v_pk_mul_f32 v[128:129], v[112:113], v[84:85]
	v_pk_mul_f32 v[136:137], v[120:121], v[86:87]
	v_pk_mul_f32 v[130:131], v[114:115], v[84:85]
	v_pk_mul_f32 v[138:139], v[122:123], v[86:87]
	v_pk_mul_f32 v[132:133], v[116:117], v[84:85]
	v_pk_mul_f32 v[140:141], v[124:125], v[86:87]
	v_pk_mul_f32 v[134:135], v[118:119], v[84:85]
	v_pk_mul_f32 v[142:143], v[126:127], v[86:87]
	v_max_f32_e32 v128, v128, v136
	v_max_f32_e32 v129, v129, v137
	v_max_f32_e32 v130, v130, v138
	v_max_f32_e32 v131, v131, v139
	v_max_f32_e32 v132, v132, v140
	v_max_f32_e32 v133, v133, v141
	v_max_f32_e32 v134, v134, v142
	v_max_f32_e32 v135, v135, v143
	v_cvt_pk_f16_f32 v148, v128, v129
	v_cvt_pk_f16_f32 v149, v130, v131
	v_cvt_pk_f16_f32 v150, v132, v133
	v_cvt_pk_f16_f32 v151, v134, v135
	s_waitcnt vmcnt(10)
	s_nop 0
	v_mfma_f32_32x32x16_f16 v[160:175], v[148:151], v[36:39], v[160:175]
	v_mfma_f32_32x32x16_f16 v[176:191], v[152:155], v[148:151], v[176:191]
	ds_read_b128 v[112:115], v3 offset:448
	ds_read_b128 v[116:119], v3 offset:464
	ds_read_b128 v[120:123], v3 offset:1472
	ds_read_b128 v[124:127], v3 offset:1488
	s_waitcnt lgkmcnt(4)
	v_pk_mul_f32 v[128:129], v[96:97], v[84:85]
	v_pk_mul_f32 v[136:137], v[104:105], v[86:87]
	v_pk_mul_f32 v[130:131], v[98:99], v[84:85]
	v_pk_mul_f32 v[138:139], v[106:107], v[86:87]
	v_pk_mul_f32 v[132:133], v[100:101], v[84:85]
	v_pk_mul_f32 v[140:141], v[108:109], v[86:87]
	v_pk_mul_f32 v[134:135], v[102:103], v[84:85]
	v_pk_mul_f32 v[142:143], v[110:111], v[86:87]
	v_max_f32_e32 v128, v128, v136
	v_max_f32_e32 v129, v129, v137
	v_max_f32_e32 v130, v130, v138
	v_max_f32_e32 v131, v131, v139
	v_max_f32_e32 v132, v132, v140
	v_max_f32_e32 v133, v133, v141
	v_max_f32_e32 v134, v134, v142
	v_max_f32_e32 v135, v135, v143
	v_cvt_pk_f16_f32 v144, v128, v129
	v_cvt_pk_f16_f32 v145, v130, v131
	v_cvt_pk_f16_f32 v146, v132, v133
	v_cvt_pk_f16_f32 v147, v134, v135
	s_waitcnt vmcnt(9)
	s_nop 0
	v_mfma_f32_32x32x16_f16 v[160:175], v[144:147], v[40:43], v[160:175]
	v_mfma_f32_32x32x16_f16 v[176:191], v[152:155], v[144:147], v[176:191]
	ds_read_b128 v[96:99], v3 offset:512
	ds_read_b128 v[100:103], v3 offset:528
	ds_read_b128 v[104:107], v3 offset:1536
	ds_read_b128 v[108:111], v3 offset:1552
	s_waitcnt lgkmcnt(4)
	v_pk_mul_f32 v[128:129], v[112:113], v[84:85]
	v_pk_mul_f32 v[136:137], v[120:121], v[86:87]
	v_pk_mul_f32 v[130:131], v[114:115], v[84:85]
	v_pk_mul_f32 v[138:139], v[122:123], v[86:87]
	v_pk_mul_f32 v[132:133], v[116:117], v[84:85]
	v_pk_mul_f32 v[140:141], v[124:125], v[86:87]
	v_pk_mul_f32 v[134:135], v[118:119], v[84:85]
	v_pk_mul_f32 v[142:143], v[126:127], v[86:87]
	v_max_f32_e32 v128, v128, v136
	v_max_f32_e32 v129, v129, v137
	v_max_f32_e32 v130, v130, v138
	v_max_f32_e32 v131, v131, v139
	v_max_f32_e32 v132, v132, v140
	v_max_f32_e32 v133, v133, v141
	v_max_f32_e32 v134, v134, v142
	v_max_f32_e32 v135, v135, v143
	v_cvt_pk_f16_f32 v148, v128, v129
	v_cvt_pk_f16_f32 v149, v130, v131
	v_cvt_pk_f16_f32 v150, v132, v133
	v_cvt_pk_f16_f32 v151, v134, v135
	s_waitcnt vmcnt(8)
	s_nop 0
	v_mfma_f32_32x32x16_f16 v[160:175], v[148:151], v[44:47], v[160:175]
	v_mfma_f32_32x32x16_f16 v[176:191], v[152:155], v[148:151], v[176:191]
	ds_read_b128 v[112:115], v3 offset:576
	ds_read_b128 v[116:119], v3 offset:592
	ds_read_b128 v[120:123], v3 offset:1600
	ds_read_b128 v[124:127], v3 offset:1616
	s_waitcnt lgkmcnt(4)
	v_pk_mul_f32 v[128:129], v[96:97], v[84:85]
	v_pk_mul_f32 v[136:137], v[104:105], v[86:87]
	v_pk_mul_f32 v[130:131], v[98:99], v[84:85]
	v_pk_mul_f32 v[138:139], v[106:107], v[86:87]
	v_pk_mul_f32 v[132:133], v[100:101], v[84:85]
	v_pk_mul_f32 v[140:141], v[108:109], v[86:87]
	v_pk_mul_f32 v[134:135], v[102:103], v[84:85]
	v_pk_mul_f32 v[142:143], v[110:111], v[86:87]
	v_max_f32_e32 v128, v128, v136
	v_max_f32_e32 v129, v129, v137
	v_max_f32_e32 v130, v130, v138
	v_max_f32_e32 v131, v131, v139
	v_max_f32_e32 v132, v132, v140
	v_max_f32_e32 v133, v133, v141
	v_max_f32_e32 v134, v134, v142
	v_max_f32_e32 v135, v135, v143
	v_cvt_pk_f16_f32 v144, v128, v129
	v_cvt_pk_f16_f32 v145, v130, v131
	v_cvt_pk_f16_f32 v146, v132, v133
	v_cvt_pk_f16_f32 v147, v134, v135
	s_waitcnt vmcnt(7)
	s_nop 0
	v_mfma_f32_32x32x16_f16 v[160:175], v[144:147], v[48:51], v[160:175]
	v_mfma_f32_32x32x16_f16 v[176:191], v[152:155], v[144:147], v[176:191]
	ds_read_b128 v[96:99], v3 offset:640
	ds_read_b128 v[100:103], v3 offset:656
	ds_read_b128 v[104:107], v3 offset:1664
	ds_read_b128 v[108:111], v3 offset:1680
	s_waitcnt lgkmcnt(4)
	v_pk_mul_f32 v[128:129], v[112:113], v[84:85]
	v_pk_mul_f32 v[136:137], v[120:121], v[86:87]
	v_pk_mul_f32 v[130:131], v[114:115], v[84:85]
	v_pk_mul_f32 v[138:139], v[122:123], v[86:87]
	v_pk_mul_f32 v[132:133], v[116:117], v[84:85]
	v_pk_mul_f32 v[140:141], v[124:125], v[86:87]
	v_pk_mul_f32 v[134:135], v[118:119], v[84:85]
	v_pk_mul_f32 v[142:143], v[126:127], v[86:87]
	v_max_f32_e32 v128, v128, v136
	v_max_f32_e32 v129, v129, v137
	v_max_f32_e32 v130, v130, v138
	v_max_f32_e32 v131, v131, v139
	v_max_f32_e32 v132, v132, v140
	v_max_f32_e32 v133, v133, v141
	v_max_f32_e32 v134, v134, v142
	v_max_f32_e32 v135, v135, v143
	v_cvt_pk_f16_f32 v148, v128, v129
	v_cvt_pk_f16_f32 v149, v130, v131
	v_cvt_pk_f16_f32 v150, v132, v133
	v_cvt_pk_f16_f32 v151, v134, v135
	s_waitcnt vmcnt(6)
	s_nop 0
	v_mfma_f32_32x32x16_f16 v[160:175], v[148:151], v[52:55], v[160:175]
	v_mfma_f32_32x32x16_f16 v[176:191], v[152:155], v[148:151], v[176:191]
	ds_read_b128 v[112:115], v3 offset:704
	ds_read_b128 v[116:119], v3 offset:720
	ds_read_b128 v[120:123], v3 offset:1728
	ds_read_b128 v[124:127], v3 offset:1744
	s_waitcnt lgkmcnt(4)
	v_pk_mul_f32 v[128:129], v[96:97], v[84:85]
	v_pk_mul_f32 v[136:137], v[104:105], v[86:87]
	v_pk_mul_f32 v[130:131], v[98:99], v[84:85]
	v_pk_mul_f32 v[138:139], v[106:107], v[86:87]
	v_pk_mul_f32 v[132:133], v[100:101], v[84:85]
	v_pk_mul_f32 v[140:141], v[108:109], v[86:87]
	v_pk_mul_f32 v[134:135], v[102:103], v[84:85]
	v_pk_mul_f32 v[142:143], v[110:111], v[86:87]
	v_max_f32_e32 v128, v128, v136
	v_max_f32_e32 v129, v129, v137
	v_max_f32_e32 v130, v130, v138
	v_max_f32_e32 v131, v131, v139
	v_max_f32_e32 v132, v132, v140
	v_max_f32_e32 v133, v133, v141
	v_max_f32_e32 v134, v134, v142
	v_max_f32_e32 v135, v135, v143
	v_cvt_pk_f16_f32 v144, v128, v129
	v_cvt_pk_f16_f32 v145, v130, v131
	v_cvt_pk_f16_f32 v146, v132, v133
	v_cvt_pk_f16_f32 v147, v134, v135
	s_waitcnt vmcnt(5)
	s_nop 0
	v_mfma_f32_32x32x16_f16 v[160:175], v[144:147], v[56:59], v[160:175]
	v_mfma_f32_32x32x16_f16 v[176:191], v[152:155], v[144:147], v[176:191]
	ds_read_b128 v[96:99], v3 offset:768
	ds_read_b128 v[100:103], v3 offset:784
	ds_read_b128 v[104:107], v3 offset:1792
	ds_read_b128 v[108:111], v3 offset:1808
	s_waitcnt lgkmcnt(4)
	v_pk_mul_f32 v[128:129], v[112:113], v[84:85]
	v_pk_mul_f32 v[136:137], v[120:121], v[86:87]
	v_pk_mul_f32 v[130:131], v[114:115], v[84:85]
	v_pk_mul_f32 v[138:139], v[122:123], v[86:87]
	v_pk_mul_f32 v[132:133], v[116:117], v[84:85]
	v_pk_mul_f32 v[140:141], v[124:125], v[86:87]
	v_pk_mul_f32 v[134:135], v[118:119], v[84:85]
	v_pk_mul_f32 v[142:143], v[126:127], v[86:87]
	v_max_f32_e32 v128, v128, v136
	v_max_f32_e32 v129, v129, v137
	v_max_f32_e32 v130, v130, v138
	v_max_f32_e32 v131, v131, v139
	v_max_f32_e32 v132, v132, v140
	v_max_f32_e32 v133, v133, v141
	v_max_f32_e32 v134, v134, v142
	v_max_f32_e32 v135, v135, v143
	v_cvt_pk_f16_f32 v148, v128, v129
	v_cvt_pk_f16_f32 v149, v130, v131
	v_cvt_pk_f16_f32 v150, v132, v133
	v_cvt_pk_f16_f32 v151, v134, v135
	s_waitcnt vmcnt(4)
	s_nop 0
	v_mfma_f32_32x32x16_f16 v[160:175], v[148:151], v[60:63], v[160:175]
	v_mfma_f32_32x32x16_f16 v[176:191], v[152:155], v[148:151], v[176:191]
	ds_read_b128 v[112:115], v3 offset:832
	ds_read_b128 v[116:119], v3 offset:848
	ds_read_b128 v[120:123], v3 offset:1856
	ds_read_b128 v[124:127], v3 offset:1872
	s_waitcnt lgkmcnt(4)
	v_pk_mul_f32 v[128:129], v[96:97], v[84:85]
	v_pk_mul_f32 v[136:137], v[104:105], v[86:87]
	v_pk_mul_f32 v[130:131], v[98:99], v[84:85]
	v_pk_mul_f32 v[138:139], v[106:107], v[86:87]
	v_pk_mul_f32 v[132:133], v[100:101], v[84:85]
	v_pk_mul_f32 v[140:141], v[108:109], v[86:87]
	v_pk_mul_f32 v[134:135], v[102:103], v[84:85]
	v_pk_mul_f32 v[142:143], v[110:111], v[86:87]
	v_max_f32_e32 v128, v128, v136
	v_max_f32_e32 v129, v129, v137
	v_max_f32_e32 v130, v130, v138
	v_max_f32_e32 v131, v131, v139
	v_max_f32_e32 v132, v132, v140
	v_max_f32_e32 v133, v133, v141
	v_max_f32_e32 v134, v134, v142
	v_max_f32_e32 v135, v135, v143
	v_cvt_pk_f16_f32 v144, v128, v129
	v_cvt_pk_f16_f32 v145, v130, v131
	v_cvt_pk_f16_f32 v146, v132, v133
	v_cvt_pk_f16_f32 v147, v134, v135
	s_waitcnt vmcnt(3)
	s_nop 0
	v_mfma_f32_32x32x16_f16 v[160:175], v[144:147], v[64:67], v[160:175]
	v_mfma_f32_32x32x16_f16 v[176:191], v[152:155], v[144:147], v[176:191]
	ds_read_b128 v[96:99], v3 offset:896
	ds_read_b128 v[100:103], v3 offset:912
	ds_read_b128 v[104:107], v3 offset:1920
	ds_read_b128 v[108:111], v3 offset:1936
	s_waitcnt lgkmcnt(4)
	v_pk_mul_f32 v[128:129], v[112:113], v[84:85]
	v_pk_mul_f32 v[136:137], v[120:121], v[86:87]
	v_pk_mul_f32 v[130:131], v[114:115], v[84:85]
	v_pk_mul_f32 v[138:139], v[122:123], v[86:87]
	v_pk_mul_f32 v[132:133], v[116:117], v[84:85]
	v_pk_mul_f32 v[140:141], v[124:125], v[86:87]
	v_pk_mul_f32 v[134:135], v[118:119], v[84:85]
	v_pk_mul_f32 v[142:143], v[126:127], v[86:87]
	v_max_f32_e32 v128, v128, v136
	v_max_f32_e32 v129, v129, v137
	v_max_f32_e32 v130, v130, v138
	v_max_f32_e32 v131, v131, v139
	v_max_f32_e32 v132, v132, v140
	v_max_f32_e32 v133, v133, v141
	v_max_f32_e32 v134, v134, v142
	v_max_f32_e32 v135, v135, v143
	v_cvt_pk_f16_f32 v148, v128, v129
	v_cvt_pk_f16_f32 v149, v130, v131
	v_cvt_pk_f16_f32 v150, v132, v133
	v_cvt_pk_f16_f32 v151, v134, v135
	s_waitcnt vmcnt(2)
	s_nop 0
	v_mfma_f32_32x32x16_f16 v[160:175], v[148:151], v[68:71], v[160:175]
	v_mfma_f32_32x32x16_f16 v[176:191], v[152:155], v[148:151], v[176:191]
	ds_read_b128 v[112:115], v3 offset:960
	ds_read_b128 v[116:119], v3 offset:976
	ds_read_b128 v[120:123], v3 offset:1984
	ds_read_b128 v[124:127], v3 offset:2000
	s_waitcnt lgkmcnt(4)
	v_pk_mul_f32 v[128:129], v[96:97], v[84:85]
	v_pk_mul_f32 v[136:137], v[104:105], v[86:87]
	v_pk_mul_f32 v[130:131], v[98:99], v[84:85]
	v_pk_mul_f32 v[138:139], v[106:107], v[86:87]
	v_pk_mul_f32 v[132:133], v[100:101], v[84:85]
	v_pk_mul_f32 v[140:141], v[108:109], v[86:87]
	v_pk_mul_f32 v[134:135], v[102:103], v[84:85]
	v_pk_mul_f32 v[142:143], v[110:111], v[86:87]
	v_max_f32_e32 v128, v128, v136
	v_max_f32_e32 v129, v129, v137
	v_max_f32_e32 v130, v130, v138
	v_max_f32_e32 v131, v131, v139
	v_max_f32_e32 v132, v132, v140
	v_max_f32_e32 v133, v133, v141
	v_max_f32_e32 v134, v134, v142
	v_max_f32_e32 v135, v135, v143
	v_cvt_pk_f16_f32 v144, v128, v129
	v_cvt_pk_f16_f32 v145, v130, v131
	v_cvt_pk_f16_f32 v146, v132, v133
	v_cvt_pk_f16_f32 v147, v134, v135
	s_waitcnt vmcnt(1)
	s_nop 0
	v_mfma_f32_32x32x16_f16 v[160:175], v[144:147], v[72:75], v[160:175]
	v_mfma_f32_32x32x16_f16 v[176:191], v[152:155], v[144:147], v[176:191]
	s_waitcnt lgkmcnt(0)
	v_pk_mul_f32 v[128:129], v[112:113], v[84:85]
	v_pk_mul_f32 v[136:137], v[120:121], v[86:87]
	v_pk_mul_f32 v[130:131], v[114:115], v[84:85]
	v_pk_mul_f32 v[138:139], v[122:123], v[86:87]
	v_pk_mul_f32 v[132:133], v[116:117], v[84:85]
	v_pk_mul_f32 v[140:141], v[124:125], v[86:87]
	v_pk_mul_f32 v[134:135], v[118:119], v[84:85]
	v_pk_mul_f32 v[142:143], v[126:127], v[86:87]
	v_max_f32_e32 v128, v128, v136
	v_max_f32_e32 v129, v129, v137
	v_max_f32_e32 v130, v130, v138
	v_max_f32_e32 v131, v131, v139
	v_max_f32_e32 v132, v132, v140
	v_max_f32_e32 v133, v133, v141
	v_max_f32_e32 v134, v134, v142
	v_max_f32_e32 v135, v135, v143
	v_cvt_pk_f16_f32 v148, v128, v129
	v_cvt_pk_f16_f32 v149, v130, v131
	v_cvt_pk_f16_f32 v150, v132, v133
	v_cvt_pk_f16_f32 v151, v134, v135
	s_waitcnt vmcnt(0)
	s_nop 0
	v_mfma_f32_32x32x16_f16 v[160:175], v[148:151], v[76:79], v[160:175]
	v_mfma_f32_32x32x16_f16 v[176:191], v[152:155], v[148:151], v[176:191]
	v_lshrrev_b32_e32 v88, 1, v3
	v_xor_b32_e32 v89, 32, v0
	v_lshlrev_b32_e32 v89, 2, v89
	s_nop 15
	v_div_scale_f32 v82, s[18:19], v176, v176, 1.0
	v_rcp_f32_e32 v83, v82
	s_nop 0
	v_fma_f32 v90, -v82, v83, 1.0
	v_fmac_f32_e32 v83, v90, v83
	v_div_scale_f32 v90, vcc, 1.0, v176, 1.0
	v_mul_f32_e32 v91, v90, v83
	v_fma_f32 v92, -v82, v91, v90
	v_fmac_f32_e32 v91, v92, v83
	v_fma_f32 v90, -v82, v91, v90
	v_div_fmas_f32 v90, v90, v83, v91
	v_div_fixup_f32 v90, v90, v176, 1.0
	ds_bpermute_b32 v96, v88, v90
	ds_bpermute_b32 v97, v88, v90 offset:4
	ds_bpermute_b32 v98, v88, v90 offset:8
	ds_bpermute_b32 v99, v88, v90 offset:12
	ds_bpermute_b32 v100, v88, v90 offset:32
	ds_bpermute_b32 v101, v88, v90 offset:36
	ds_bpermute_b32 v102, v88, v90 offset:40
	ds_bpermute_b32 v103, v88, v90 offset:44
	ds_bpermute_b32 v104, v88, v90 offset:64
	ds_bpermute_b32 v105, v88, v90 offset:68
	ds_bpermute_b32 v106, v88, v90 offset:72
	ds_bpermute_b32 v107, v88, v90 offset:76
	ds_bpermute_b32 v108, v88, v90 offset:96
	ds_bpermute_b32 v109, v88, v90 offset:100
	ds_bpermute_b32 v110, v88, v90 offset:104
	ds_bpermute_b32 v111, v88, v90 offset:108
	s_waitcnt vmcnt(0)
	s_waitcnt lgkmcnt(0)
	v_fma_f32 v112, v160, v96, v9
	v_fma_f32 v113, v161, v97, v9
	v_fma_f32 v114, v162, v98, v9
	v_fma_f32 v115, v163, v99, v9
	v_fma_f32 v116, v164, v100, v9
	v_fma_f32 v117, v165, v101, v9
	v_fma_f32 v118, v166, v102, v9
	v_fma_f32 v119, v167, v103, v9
	v_fma_f32 v120, v168, v104, v9
	v_fma_f32 v121, v169, v105, v9
	v_fma_f32 v122, v170, v106, v9
	v_fma_f32 v123, v171, v107, v9
	v_fma_f32 v124, v172, v108, v9
	v_fma_f32 v125, v173, v109, v9
	v_fma_f32 v126, v174, v110, v9
	v_fma_f32 v127, v175, v111, v9
	v_max_f32_e32 v112, 0, v112
	v_max_f32_e32 v113, 0, v113
	v_max_f32_e32 v114, 0, v114
	v_max_f32_e32 v115, 0, v115
	v_max_f32_e32 v116, 0, v116
	v_max_f32_e32 v117, 0, v117
	v_max_f32_e32 v118, 0, v118
	v_max_f32_e32 v119, 0, v119
	v_max_f32_e32 v120, 0, v120
	v_max_f32_e32 v121, 0, v121
	v_max_f32_e32 v122, 0, v122
	v_max_f32_e32 v123, 0, v123
	v_max_f32_e32 v124, 0, v124
	v_max_f32_e32 v125, 0, v125
	v_max_f32_e32 v126, 0, v126
	v_max_f32_e32 v127, 0, v127
	v_add_f32_e32 v82, 0, v112
	v_add_f32_e32 v82, v82, v113
	v_add_f32_e32 v82, v82, v114
	v_add_f32_e32 v82, v82, v115
	v_add_f32_e32 v82, v82, v116
	v_add_f32_e32 v82, v82, v117
	v_add_f32_e32 v82, v82, v118
	v_add_f32_e32 v82, v82, v119
	v_add_f32_e32 v82, v82, v120
	v_add_f32_e32 v82, v82, v121
	v_add_f32_e32 v82, v82, v122
	v_add_f32_e32 v82, v82, v123
	v_add_f32_e32 v82, v82, v124
	v_add_f32_e32 v82, v82, v125
	v_add_f32_e32 v82, v82, v126
	v_add_f32_e32 v82, v82, v127
	ds_bpermute_b32 v83, v89, v82
	v_cmp_gt_u32_e32 vcc, 32, v0
	s_and_saveexec_b64 s[18:19], vcc
	s_cbranch_execz .Lg3s_end
	s_waitcnt lgkmcnt(0)
	v_add_f32_e32 v82, v82, v83
	global_atomic_add_f32 v10, v82, s[10:11]

	.amdhsa_kernel _Z12gat3s_kernelPKfPKDF16_S0_Pf
		.amdhsa_group_segment_fixed_size 2048
		.amdhsa_private_segment_fixed_size 0
		.amdhsa_kernarg_size 32
		.amdhsa_user_sgpr_count 2
		.amdhsa_user_sgpr_dispatch_ptr 0
		.amdhsa_user_sgpr_queue_ptr 0
		.amdhsa_user_sgpr_kernarg_segment_ptr 1
		.amdhsa_user_sgpr_dispatch_id 0
		.amdhsa_user_sgpr_kernarg_preload_length 0
		.amdhsa_user_sgpr_kernarg_preload_offset 0
		.amdhsa_user_sgpr_private_segment_size 0
		.amdhsa_uses_dynamic_stack 0
		.amdhsa_enable_private_segment 0
		.amdhsa_system_sgpr_workgroup_id_x 1
		.amdhsa_system_sgpr_workgroup_id_y 0
		.amdhsa_system_sgpr_workgroup_id_z 0
		.amdhsa_system_sgpr_workgroup_info 0
		.amdhsa_system_vgpr_workitem_id 0
		.amdhsa_next_free_vgpr 192
		.amdhsa_next_free_sgpr 20
		.amdhsa_accum_offset 192
		.amdhsa_reserve_vcc 1
		.amdhsa_float_round_mode_32 0
		.amdhsa_float_round_mode_16_64 0
		.amdhsa_float_denorm_mode_32 3
		.amdhsa_float_denorm_mode_16_64 3
		.amdhsa_dx10_clamp 1
		.amdhsa_ieee_mode 1
		.amdhsa_fp16_overflow 0
		.amdhsa_tg_split 0
		.amdhsa_exception_fp_ieee_invalid_op 0
		.amdhsa_exception_fp_denorm_src 0
		.amdhsa_exception_fp_ieee_div_zero 0
		.amdhsa_exception_fp_ieee_overflow 0
		.amdhsa_exception_fp_ieee_underflow 0
		.amdhsa_exception_fp_ieee_inexact 0
		.amdhsa_exception_int_div_zero 0
	.end_amdhsa_kernel

.LBB10_4:
	s_or_b64 exec, exec, s[6:7]
	v_and_b32_e32 v222, 1, v5
	v_bfe_u32 v3, v219, 1, 1
	v_lshrrev_b32_e32 v2, 1, v219
	v_bfe_u32 v223, v0, 5, 1
	v_lshl_or_b32 v225, v222, 3, v3
	v_mov_b32_e32 v3, 0x14400
	v_lshl_add_u32 v226, v4, 7, v3
	v_bitop3_b32 v3, v2, v223, 7 bitop3:0x6c
	s_load_dwordx2 s[0:1], s[0:1], 0x18
	v_and_b32_e32 v5, 1, v0
	v_lshlrev_b32_e32 v227, 4, v3
	v_or_b32_e32 v3, 2, v223
	v_and_or_b32 v224, v6, 14, v5
	v_bfe_u32 v5, v219, 1, 3
	v_bitop3_b32 v2, v2, v3, 7 bitop3:0x6c
	v_lshlrev_b32_e32 v228, 4, v2
	v_bitop3_b32 v2, v223, v5, 4 bitop3:0x36
	v_lshlrev_b32_e32 v229, 4, v2
	v_bitop3_b32 v2, v223, v5, 6 bitop3:0x36
	v_mov_b32_e32 v66, 0
	v_mov_b32_e32 v154, 0
	v_lshlrev_b32_e32 v230, 4, v2
	s_mov_b32 s5, 0
	s_mov_b64 s[6:7], 0x6000
	s_mov_b64 s[8:9], 0x4000
	s_mov_b64 s[10:11], 0x2000
	s_mov_b32 s4, 0
	s_mov_b32 s14, 0
	s_mov_b32 s15, 0
	v_mov_b32_e32 v155, v154
	v_mov_b32_e32 v156, v154
	v_mov_b32_e32 v157, v154
	v_mov_b32_e32 v158, v154
	v_mov_b32_e32 v159, v154
	v_mov_b32_e32 v160, v154
	v_mov_b32_e32 v161, v154
	v_mov_b32_e32 v162, v154
	v_mov_b32_e32 v163, v154
	v_mov_b32_e32 v164, v154
	v_mov_b32_e32 v165, v154
	v_mov_b32_e32 v170, v154
	v_mov_b32_e32 v171, v154
	v_mov_b32_e32 v172, v154
	v_mov_b32_e32 v173, v154
	v_mov_b32_e32 v150, v154
	v_mov_b32_e32 v151, v154
	v_mov_b32_e32 v152, v154
	v_mov_b32_e32 v153, v154
	v_mov_b32_e32 v138, v154
	v_mov_b32_e32 v139, v154
	v_mov_b32_e32 v140, v154
	v_mov_b32_e32 v141, v154
	v_mov_b32_e32 v134, v154
	v_mov_b32_e32 v135, v154
	v_mov_b32_e32 v136, v154
	v_mov_b32_e32 v137, v154
	v_mov_b32_e32 v130, v154
	v_mov_b32_e32 v131, v154
	v_mov_b32_e32 v132, v154
	v_mov_b32_e32 v133, v154
	v_mov_b32_e32 v67, v66
	v_mov_b32_e32 v68, v66
	v_mov_b32_e32 v69, v66
	v_mov_b32_e32 v70, v66
	v_mov_b32_e32 v71, v66
	v_mov_b32_e32 v72, v66
	v_mov_b32_e32 v73, v66
	v_mov_b32_e32 v74, v66
	v_mov_b32_e32 v75, v66
	v_mov_b32_e32 v76, v66
	v_mov_b32_e32 v77, v66
	v_mov_b32_e32 v78, v66
	v_mov_b32_e32 v79, v66
	v_mov_b32_e32 v80, v66
	v_mov_b32_e32 v81, v66
	v_mov_b32_e32 v34, v66
	v_mov_b32_e32 v35, v66
	v_mov_b32_e32 v36, v66
	v_mov_b32_e32 v37, v66
	v_mov_b32_e32 v38, v66
	v_mov_b32_e32 v39, v66
	v_mov_b32_e32 v40, v66
	v_mov_b32_e32 v41, v66
	v_mov_b32_e32 v42, v66
	v_mov_b32_e32 v43, v66
	v_mov_b32_e32 v44, v66
	v_mov_b32_e32 v45, v66
	v_mov_b32_e32 v46, v66
	v_mov_b32_e32 v47, v66
	v_mov_b32_e32 v48, v66
	v_mov_b32_e32 v49, v66
	v_mov_b32_e32 v82, v66
	v_mov_b32_e32 v83, v66
	v_mov_b32_e32 v84, v66
	v_mov_b32_e32 v85, v66
	v_mov_b32_e32 v86, v66
	v_mov_b32_e32 v87, v66
	v_mov_b32_e32 v88, v66
	v_mov_b32_e32 v89, v66
	v_mov_b32_e32 v90, v66
	v_mov_b32_e32 v91, v66
	v_mov_b32_e32 v92, v66
	v_mov_b32_e32 v93, v66
	v_mov_b32_e32 v94, v66
	v_mov_b32_e32 v95, v66
	v_mov_b32_e32 v96, v66
	v_mov_b32_e32 v97, v66
	v_mov_b32_e32 v2, v66
	v_mov_b32_e32 v3, v66
	v_mov_b32_e32 v4, v66
	v_mov_b32_e32 v5, v66
	v_mov_b32_e32 v6, v66
	v_mov_b32_e32 v7, v66
	v_mov_b32_e32 v8, v66
	v_mov_b32_e32 v9, v66
	v_mov_b32_e32 v10, v66
	v_mov_b32_e32 v11, v66
	v_mov_b32_e32 v12, v66
	v_mov_b32_e32 v13, v66
	v_mov_b32_e32 v14, v66
	v_mov_b32_e32 v15, v66
	v_mov_b32_e32 v16, v66
	v_mov_b32_e32 v17, v66
	v_mov_b32_e32 v142, v154
	v_mov_b32_e32 v143, v154
	v_mov_b32_e32 v144, v154
	v_mov_b32_e32 v145, v154
	v_mov_b32_e32 v146, v154
	v_mov_b32_e32 v147, v154
	v_mov_b32_e32 v148, v154
	v_mov_b32_e32 v149, v154
	v_mov_b32_e32 v166, v154
	v_mov_b32_e32 v167, v154
	v_mov_b32_e32 v168, v154
	v_mov_b32_e32 v169, v154
	v_mov_b32_e32 v174, v154
	v_mov_b32_e32 v175, v154
	v_mov_b32_e32 v176, v154
	v_mov_b32_e32 v177, v154
	v_mov_b32_e32 v114, v66
	v_mov_b32_e32 v115, v66
	v_mov_b32_e32 v116, v66
	v_mov_b32_e32 v117, v66
	v_mov_b32_e32 v118, v66
	v_mov_b32_e32 v119, v66
	v_mov_b32_e32 v120, v66
	v_mov_b32_e32 v121, v66
	v_mov_b32_e32 v122, v66
	v_mov_b32_e32 v123, v66
	v_mov_b32_e32 v124, v66
	v_mov_b32_e32 v125, v66
	v_mov_b32_e32 v126, v66
	v_mov_b32_e32 v127, v66
	v_mov_b32_e32 v128, v66
	v_mov_b32_e32 v129, v66
	v_mov_b32_e32 v50, v66
	v_mov_b32_e32 v51, v66
	v_mov_b32_e32 v52, v66
	v_mov_b32_e32 v53, v66
	v_mov_b32_e32 v54, v66
	v_mov_b32_e32 v55, v66
	v_mov_b32_e32 v56, v66
	v_mov_b32_e32 v57, v66
	v_mov_b32_e32 v58, v66
	v_mov_b32_e32 v59, v66
	v_mov_b32_e32 v60, v66
	v_mov_b32_e32 v61, v66
	v_mov_b32_e32 v62, v66
	v_mov_b32_e32 v63, v66
	v_mov_b32_e32 v64, v66
	v_mov_b32_e32 v65, v66
	v_mov_b32_e32 v98, v66
	v_mov_b32_e32 v99, v66
	v_mov_b32_e32 v100, v66
	v_mov_b32_e32 v101, v66
	v_mov_b32_e32 v102, v66
	v_mov_b32_e32 v103, v66
	v_mov_b32_e32 v104, v66
	v_mov_b32_e32 v105, v66
	v_mov_b32_e32 v106, v66
	v_mov_b32_e32 v107, v66
	v_mov_b32_e32 v108, v66
	v_mov_b32_e32 v109, v66
	v_mov_b32_e32 v110, v66
	v_mov_b32_e32 v111, v66
	v_mov_b32_e32 v112, v66
	v_mov_b32_e32 v113, v66
	v_mov_b32_e32 v18, v66
	v_mov_b32_e32 v19, v66
	v_mov_b32_e32 v20, v66
	v_mov_b32_e32 v21, v66
	v_mov_b32_e32 v22, v66
	v_mov_b32_e32 v23, v66
	v_mov_b32_e32 v24, v66
	v_mov_b32_e32 v25, v66
	v_mov_b32_e32 v26, v66
	v_mov_b32_e32 v27, v66
	v_mov_b32_e32 v28, v66
	v_mov_b32_e32 v29, v66
	v_mov_b32_e32 v30, v66
	v_mov_b32_e32 v31, v66
	v_mov_b32_e32 v32, v66
	v_mov_b32_e32 v33, v66
	s_waitcnt vmcnt(0) lgkmcnt(0)
	s_barrier
	s_branch .LBB10_6

.LBB10_8:
	s_waitcnt lgkmcnt(0)
	v_mfma_f32_32x32x16_f16 v[66:81], v[170:173], v[174:177], v[66:81]
	v_or_b32_e32 v1, 0x600, v0
	v_lshrrev_b32_e32 v178, 3, v1
	s_lshl_b32 s4, s13, 8
	v_and_b32_e32 v178, 0xe0, v178
	v_bfe_u32 v179, v0, 5, 3
	s_lshl_b64 s[2:3], s[2:3], 10
	v_or_b32_e32 v178, s4, v178
	v_mfma_f32_32x32x16_f16 v[66:81], v[150:153], v[146:149], v[66:81]
	v_lshl_or_b32 v183, s12, 3, v179
	v_or3_b32 v180, s2, v178, v183
	v_mov_b32_e32 v181, s3
	v_lshlrev_b64 v[178:179], 9, v[180:181]
	v_lshlrev_b32_e32 v1, 4, v1
	s_movk_i32 s3, 0x7e00
	v_lshl_add_u64 v[178:179], s[0:1], 0, v[178:179]
	v_mfma_f32_32x32x16_f16 v[82:97], v[162:165], v[174:177], v[82:97]
	s_nop 3
	v_fma_f32 v66, v221, v66, v220
	v_fma_f32 v67, v221, v67, v220
	v_fma_f32 v68, v221, v68, v220
	v_fma_f32 v69, v221, v69, v220
	v_max_f32_e32 v66, v66, v67
	v_max_f32_e32 v67, v68, v69
	v_max3_f32 v66, v66, v67, 0
	v_fma_f32 v67, v221, v70, v220
	v_fma_f32 v68, v221, v71, v220
	v_fma_f32 v69, v221, v72, v220
	v_fma_f32 v70, v221, v73, v220
	v_mfma_f32_32x32x16_f16 v[82:97], v[138:141], v[146:149], v[82:97]
	v_max_f32_e32 v67, v67, v68
	v_max_f32_e32 v68, v69, v70
	v_max3_f32 v67, v67, v68, 0
	v_fma_f32 v68, v221, v74, v220
	v_fma_f32 v69, v221, v75, v220
	v_fma_f32 v70, v221, v76, v220
	v_fma_f32 v71, v221, v77, v220
	v_mfma_f32_32x32x16_f16 v[114:129], v[158:161], v[174:177], v[114:129]
	v_max_f32_e32 v68, v68, v69
	v_max_f32_e32 v69, v70, v71
	v_cvt_f16_f32_e32 v66, v66
	v_max3_f32 v68, v68, v69, 0
	v_fma_f32 v69, v221, v78, v220
	v_fma_f32 v70, v221, v79, v220
	v_fma_f32 v71, v221, v80, v220
	v_mfma_f32_32x32x16_f16 v[50:65], v[158:161], v[166:169], v[50:65]
	v_lshlrev_b32_e32 v159, 1, v219
	v_fma_f32 v72, v221, v81, v220
	v_lshl_add_u32 v159, v218, 1, v159
	v_cvt_f16_f32_e32 v67, v67
	v_max_f32_e32 v69, v69, v70
	v_max_f32_e32 v70, v71, v72
	v_lshl_or_b32 v159, v222, 14, v159
	v_cvt_f16_f32_e32 v68, v68
	v_max3_f32 v69, v69, v70, 0
	v_lshl_add_u32 v159, v223, 9, v159
	v_cvt_f16_f32_e32 v69, v69
	ds_write_b16 v159, v66
	ds_write_b16 v159, v67 offset:1024
	ds_write_b16 v159, v68 offset:2048
	ds_write_b16 v159, v69 offset:3072
	v_fma_f32 v66, v221, v82, v220
	v_fma_f32 v67, v221, v83, v220
	v_fma_f32 v68, v221, v84, v220
	v_fma_f32 v69, v221, v85, v220
	v_max_f32_e32 v66, v66, v67
	v_max_f32_e32 v67, v68, v69
	v_mfma_f32_32x32x16_f16 v[114:129], v[134:137], v[146:149], v[114:129]
	v_max3_f32 v66, v66, v67, 0
	v_fma_f32 v67, v221, v86, v220
	v_fma_f32 v68, v221, v87, v220
	v_fma_f32 v69, v221, v88, v220
	v_fma_f32 v70, v221, v89, v220
	v_max_f32_e32 v67, v67, v68
	v_max_f32_e32 v68, v69, v70
	v_mfma_f32_32x32x16_f16 v[34:49], v[170:173], v[166:169], v[34:49]
	v_max3_f32 v67, v67, v68, 0
	v_fma_f32 v68, v221, v90, v220
	v_fma_f32 v69, v221, v91, v220
	v_fma_f32 v70, v221, v92, v220
	v_fma_f32 v71, v221, v93, v220
	v_max_f32_e32 v68, v68, v69
	v_max_f32_e32 v69, v70, v71
	v_mfma_f32_32x32x16_f16 v[2:17], v[162:165], v[166:169], v[2:17]
	v_cvt_f16_f32_e32 v66, v66
	v_max3_f32 v68, v68, v69, 0
	v_fma_f32 v69, v221, v94, v220
	v_fma_f32 v70, v221, v95, v220
	v_fma_f32 v71, v221, v96, v220
	v_fma_f32 v72, v221, v97, v220
	v_cvt_f16_f32_e32 v67, v67
	v_mfma_f32_32x32x16_f16 v[98:113], v[154:157], v[174:177], v[98:113]
	v_max_f32_e32 v69, v69, v70
	v_max_f32_e32 v70, v71, v72
	v_cvt_f16_f32_e32 v68, v68
	v_max3_f32 v69, v69, v70, 0
	v_cvt_f16_f32_e32 v69, v69
	ds_write_b16 v159, v66 offset:4096
	ds_write_b16 v159, v67 offset:5120
	ds_write_b16 v159, v68 offset:6144
	ds_write_b16 v159, v69 offset:7168
	v_fma_f32 v66, v221, v114, v220
	v_fma_f32 v67, v221, v115, v220
	v_fma_f32 v68, v221, v116, v220
	v_fma_f32 v69, v221, v117, v220
	v_max_f32_e32 v66, v66, v67
	v_max_f32_e32 v67, v68, v69
	v_mfma_f32_32x32x16_f16 v[34:49], v[150:153], v[142:145], v[34:49]
	v_max3_f32 v66, v66, v67, 0
	v_fma_f32 v67, v221, v118, v220
	v_fma_f32 v68, v221, v119, v220
	v_fma_f32 v69, v221, v120, v220
	v_fma_f32 v70, v221, v121, v220
	v_max_f32_e32 v67, v67, v68
	v_max_f32_e32 v68, v69, v70
	v_mfma_f32_32x32x16_f16 v[2:17], v[138:141], v[142:145], v[2:17]
	v_max3_f32 v67, v67, v68, 0
	v_fma_f32 v68, v221, v122, v220
	v_fma_f32 v69, v221, v123, v220
	v_fma_f32 v70, v221, v124, v220
	v_fma_f32 v71, v221, v125, v220
	v_max_f32_e32 v68, v68, v69
	v_max_f32_e32 v69, v70, v71
	v_mfma_f32_32x32x16_f16 v[98:113], v[130:133], v[146:149], v[98:113]
	v_cvt_f16_f32_e32 v66, v66
	v_max3_f32 v68, v68, v69, 0
	v_fma_f32 v69, v221, v126, v220
	v_fma_f32 v70, v221, v127, v220
	v_fma_f32 v71, v221, v128, v220
	v_fma_f32 v72, v221, v129, v220
	v_cvt_f16_f32_e32 v67, v67
	v_max_f32_e32 v69, v69, v70
	v_max_f32_e32 v70, v71, v72
	v_cvt_f16_f32_e32 v68, v68
	v_max3_f32 v69, v69, v70, 0
	v_cvt_f16_f32_e32 v69, v69
	ds_write_b16 v159, v66 offset:8192
	ds_write_b16 v159, v67 offset:9216
	ds_write_b16 v159, v68 offset:10240
	ds_write_b16 v159, v69 offset:11264
	v_fma_f32 v66, v221, v98, v220
	v_fma_f32 v67, v221, v99, v220
	v_fma_f32 v68, v221, v100, v220
	v_fma_f32 v69, v221, v101, v220
	v_fma_f32 v34, v217, v34, v216
	v_fma_f32 v35, v217, v35, v216
	v_fma_f32 v36, v217, v36, v216
	v_fma_f32 v37, v217, v37, v216
	v_fma_f32 v2, v217, v2, v216
	v_fma_f32 v3, v217, v3, v216
	v_fma_f32 v4, v217, v4, v216
	v_fma_f32 v5, v217, v5, v216
	v_max_f32_e32 v66, v66, v67
	v_max_f32_e32 v67, v68, v69
	v_max_f32_e32 v34, v34, v35
	v_max_f32_e32 v35, v36, v37
	v_max_f32_e32 v2, v2, v3
	v_max_f32_e32 v3, v4, v5
	v_mfma_f32_32x32x16_f16 v[50:65], v[134:137], v[142:145], v[50:65]
	v_max3_f32 v66, v66, v67, 0
	v_fma_f32 v67, v221, v102, v220
	v_fma_f32 v68, v221, v103, v220
	v_fma_f32 v69, v221, v104, v220
	v_fma_f32 v70, v221, v105, v220
	v_max3_f32 v34, v34, v35, 0
	v_fma_f32 v35, v217, v38, v216
	v_fma_f32 v36, v217, v39, v216
	v_fma_f32 v37, v217, v40, v216
	v_fma_f32 v38, v217, v41, v216
	v_max3_f32 v2, v2, v3, 0
	v_fma_f32 v3, v217, v6, v216
	v_fma_f32 v4, v217, v7, v216
	v_fma_f32 v5, v217, v8, v216
	v_fma_f32 v6, v217, v9, v216
	v_max_f32_e32 v67, v67, v68
	v_max_f32_e32 v68, v69, v70
	v_max_f32_e32 v35, v35, v36
	v_max_f32_e32 v36, v37, v38
	v_max_f32_e32 v3, v3, v4
	v_max_f32_e32 v4, v5, v6
	v_mfma_f32_32x32x16_f16 v[18:33], v[154:157], v[166:169], v[18:33]
	v_max3_f32 v67, v67, v68, 0
	v_fma_f32 v68, v221, v106, v220
	v_fma_f32 v69, v221, v107, v220
	v_fma_f32 v70, v221, v108, v220
	v_fma_f32 v71, v221, v109, v220
	v_max3_f32 v35, v35, v36, 0
	v_fma_f32 v36, v217, v42, v216
	v_fma_f32 v37, v217, v43, v216
	v_fma_f32 v38, v217, v44, v216
	v_fma_f32 v39, v217, v45, v216
	v_max3_f32 v3, v3, v4, 0
	v_fma_f32 v4, v217, v10, v216
	v_fma_f32 v5, v217, v11, v216
	v_fma_f32 v6, v217, v12, v216
	v_fma_f32 v7, v217, v13, v216
	v_max_f32_e32 v68, v68, v69
	v_max_f32_e32 v69, v70, v71
	v_max_f32_e32 v36, v36, v37
	v_max_f32_e32 v37, v38, v39
	v_max_f32_e32 v4, v4, v5
	v_max_f32_e32 v5, v6, v7
	v_cvt_f16_f32_e32 v66, v66
	v_max3_f32 v68, v68, v69, 0
	v_fma_f32 v69, v221, v110, v220
	v_fma_f32 v70, v221, v111, v220
	v_fma_f32 v71, v221, v112, v220
	v_fmac_f32_e32 v220, v221, v113
	v_cvt_f16_f32_e32 v34, v34
	v_max3_f32 v36, v36, v37, 0
	v_fma_f32 v37, v217, v46, v216
	v_fma_f32 v38, v217, v47, v216
	v_fma_f32 v39, v217, v48, v216
	v_fma_f32 v40, v217, v49, v216
	v_cvt_f16_f32_e32 v2, v2
	v_max3_f32 v4, v4, v5, 0
	v_fma_f32 v5, v217, v14, v216
	v_fma_f32 v6, v217, v15, v216
	v_fma_f32 v7, v217, v16, v216
	v_fma_f32 v8, v217, v17, v216
	v_cvt_f16_f32_e32 v67, v67
	v_max_f32_e32 v69, v69, v70
	v_max_f32_e32 v70, v71, v220
	v_cvt_f16_f32_e32 v35, v35
	v_max_f32_e32 v37, v37, v38
	v_max_f32_e32 v38, v39, v40
	v_cvt_f16_f32_e32 v3, v3
	v_max_f32_e32 v5, v5, v6
	v_max_f32_e32 v6, v7, v8
	v_cvt_f16_f32_e32 v68, v68
	v_max3_f32 v69, v69, v70, 0
	v_cvt_f16_f32_e32 v36, v36
	v_max3_f32 v37, v37, v38, 0
	v_cvt_f16_f32_e32 v4, v4
	v_max3_f32 v5, v5, v6, 0
	v_cvt_f16_f32_e32 v69, v69
	v_cvt_f16_f32_e32 v37, v37
	v_cvt_f16_f32_e32 v5, v5
	ds_write_b16 v159, v66 offset:12288
	ds_write_b16 v159, v67 offset:13312
	ds_write_b16 v159, v68 offset:14336
	ds_write_b16 v159, v69 offset:15360
	ds_write_b16 v159, v34 offset:64
	ds_write_b16 v159, v35 offset:1088
	ds_write_b16 v159, v36 offset:2112
	ds_write_b16 v159, v37 offset:3136
	ds_write_b16 v159, v2 offset:4160
	ds_write_b16 v159, v3 offset:5184
	ds_write_b16 v159, v4 offset:6208
	ds_write_b16 v159, v5 offset:7232
	v_fma_f32 v2, v217, v50, v216
	v_fma_f32 v3, v217, v51, v216
	v_fma_f32 v4, v217, v52, v216
	v_fma_f32 v5, v217, v53, v216
	v_max_f32_e32 v2, v2, v3
	v_max_f32_e32 v3, v4, v5
	v_mfma_f32_32x32x16_f16 v[18:33], v[130:133], v[142:145], v[18:33]
	v_max3_f32 v2, v2, v3, 0
	v_fma_f32 v3, v217, v54, v216
	v_fma_f32 v4, v217, v55, v216
	v_fma_f32 v5, v217, v56, v216
	v_fma_f32 v6, v217, v57, v216
	v_max_f32_e32 v3, v3, v4
	v_max_f32_e32 v4, v5, v6
	v_max3_f32 v3, v3, v4, 0
	v_fma_f32 v4, v217, v58, v216
	v_fma_f32 v5, v217, v59, v216
	v_fma_f32 v6, v217, v60, v216
	v_fma_f32 v7, v217, v61, v216
	v_max_f32_e32 v4, v4, v5
	v_max_f32_e32 v5, v6, v7
	v_cvt_f16_f32_e32 v2, v2
	v_max3_f32 v4, v4, v5, 0
	v_fma_f32 v5, v217, v62, v216
	v_fma_f32 v6, v217, v63, v216
	v_fma_f32 v7, v217, v64, v216
	v_fma_f32 v8, v217, v65, v216
	v_cvt_f16_f32_e32 v3, v3
	v_max_f32_e32 v5, v5, v6
	v_max_f32_e32 v6, v7, v8
	v_cvt_f16_f32_e32 v4, v4
	v_max3_f32 v5, v5, v6, 0
	v_cvt_f16_f32_e32 v5, v5
	ds_write_b16 v159, v2 offset:8256
	ds_write_b16 v159, v3 offset:9280
	ds_write_b16 v159, v4 offset:10304
	ds_write_b16 v159, v5 offset:11328
	v_fma_f32 v2, v217, v18, v216
	v_fma_f32 v3, v217, v19, v216
	v_fma_f32 v4, v217, v20, v216
	v_fma_f32 v5, v217, v21, v216
	v_max_f32_e32 v2, v2, v3
	v_max_f32_e32 v3, v4, v5
	v_max3_f32 v2, v2, v3, 0
	v_fma_f32 v3, v217, v22, v216
	v_fma_f32 v4, v217, v23, v216
	v_fma_f32 v5, v217, v24, v216
	v_fma_f32 v6, v217, v25, v216
	v_lshlrev_b32_e32 v172, 4, v219
	v_max_f32_e32 v3, v3, v4
	v_max_f32_e32 v4, v5, v6
	v_mov_b32_e32 v173, 0
	v_and_or_b32 v184, v1, s3, v172
	v_or_b32_e32 v1, 0x400, v0
	v_max3_f32 v3, v3, v4, 0
	v_fma_f32 v4, v217, v26, v216
	v_fma_f32 v5, v217, v27, v216
	v_fma_f32 v6, v217, v28, v216
	v_fma_f32 v7, v217, v29, v216
	v_lshl_add_u64 v[170:171], v[178:179], 0, v[172:173]
	v_lshrrev_b32_e32 v178, 3, v1
	v_lshlrev_b32_e32 v1, 4, v1
	s_movk_i32 s3, 0x5e00
	v_max_f32_e32 v4, v4, v5
	v_max_f32_e32 v5, v6, v7
	v_and_or_b32 v164, v1, s3, v172
	v_or_b32_e32 v1, 0x200, v0
	v_cvt_f16_f32_e32 v2, v2
	v_max3_f32 v4, v4, v5, 0
	v_fma_f32 v5, v217, v30, v216
	v_fma_f32 v6, v217, v31, v216
	v_fma_f32 v7, v217, v32, v216
	v_fmac_f32_e32 v216, v217, v33
	v_and_b32_e32 v178, 0xa0, v178
	v_lshrrev_b32_e32 v162, 3, v1
	v_cvt_f16_f32_e32 v3, v3
	v_max_f32_e32 v5, v5, v6
	v_max_f32_e32 v6, v7, v216
	v_lshrrev_b32_e32 v182, 5, v0
	v_or_b32_e32 v178, s4, v178
	v_and_b32_e32 v162, 0x60, v162
	v_cvt_f16_f32_e32 v4, v4
	v_max3_f32 v5, v5, v6, 0
	v_or3_b32 v180, s2, v178, v183
	v_or_b32_e32 v162, s4, v162
	v_lshlrev_b32_e32 v1, 4, v1
	s_movk_i32 s3, 0x3e00
	v_lshrrev_b32_e32 v0, 3, v0
	v_lshl_or_b32 v158, v182, 9, v172
	v_cvt_f16_f32_e32 v5, v5
	v_lshlrev_b64 v[178:179], 9, v[180:181]
	v_or3_b32 v180, s2, v162, v183
	v_and_or_b32 v165, v1, s3, v172
	v_and_or_b32 v0, v0, 32, s4
	ds_write_b16 v159, v2 offset:12352
	ds_write_b16 v159, v3 offset:13376
	ds_write_b16 v159, v4 offset:14400
	ds_write_b16 v159, v5 offset:15424
	s_waitcnt vmcnt(0) lgkmcnt(0)
	s_barrier
	ds_read_b128 v[2:5], v158
	ds_read_b128 v[6:9], v165
	ds_read_b128 v[10:13], v164
	ds_read_b128 v[14:17], v184
	v_lshlrev_b64 v[162:163], 9, v[180:181]
	v_or3_b32 v180, s2, v0, v183
	v_lshlrev_b64 v[0:1], 9, v[180:181]
	v_lshl_add_u64 v[0:1], s[0:1], 0, v[0:1]
	v_lshl_add_u64 v[178:179], s[0:1], 0, v[178:179]
	v_lshl_add_u64 v[162:163], s[0:1], 0, v[162:163]
	v_lshl_add_u64 v[0:1], v[0:1], 0, v[172:173]
	v_lshl_add_u64 v[178:179], v[178:179], 0, v[172:173]
	v_lshl_add_u64 v[162:163], v[162:163], 0, v[172:173]
	s_waitcnt lgkmcnt(3)
	global_store_dwordx4 v[0:1], v[2:5], off sc0 sc1
	s_waitcnt lgkmcnt(2)
	global_store_dwordx4 v[162:163], v[6:9], off sc0 sc1
	s_waitcnt lgkmcnt(1)
	global_store_dwordx4 v[178:179], v[10:13], off sc0 sc1
	s_waitcnt lgkmcnt(0)
	global_store_dwordx4 v[170:171], v[14:17], off sc0 sc1
	s_endpgm
	s_endpgm
	s_endpgm
	s_endpgm
	s_endpgm
	s_endpgm
	s_endpgm
	s_endpgm
	s_endpgm
	s_endpgm
	s_endpgm
	s_endpgm
	s_endpgm
	s_endpgm
	s_endpgm
	s_endpgm
	s_endpgm
	s_endpgm
	s_endpgm
	s_endpgm
	s_endpgm
	s_endpgm
	s_endpgm
	s_endpgm
	s_endpgm
	s_endpgm
	s_endpgm
	s_endpgm
	s_endpgm
	s_endpgm
	s_endpgm
	s_endpgm
	s_endpgm
	s_endpgm
	s_endpgm
	s_endpgm
	s_endpgm
	s_endpgm
	s_endpgm
	s_endpgm
	s_endpgm
	s_endpgm
	s_endpgm
	s_endpgm
	s_endpgm
	s_endpgm
	s_endpgm
	s_endpgm
	s_endpgm
	s_endpgm
	s_endpgm
	s_endpgm
	s_endpgm
	s_endpgm
	s_endpgm
	s_endpgm
	s_endpgm

.LBB11_4:
	s_or_b64 exec, exec, s[0:1]
	v_and_b32_e32 v98, 1, v14
	v_lshrrev_b32_e32 v2, 1, v94
	v_and_b32_e32 v4, 1, v0
	v_and_or_b32 v102, v12, 14, v4
	v_bfe_u32 v4, v94, 1, 3
	v_bitop3_b32 v2, v2, v98, 7 bitop3:0x6c
	v_lshlrev_b32_e32 v105, 4, v2
	v_bitop3_b32 v2, v98, v4, 2 bitop3:0x36
	v_bfe_u32 v3, v94, 1, 1
	v_and_b32_e32 v100, 1, v10
	v_lshlrev_b32_e32 v106, 4, v2
	v_bitop3_b32 v2, v98, v4, 4 bitop3:0x36
	v_lshrrev_b32_e32 v101, 8, v0
	v_lshl_or_b32 v103, v100, 2, v3
	v_lshlrev_b32_e32 v3, 7, v11
	v_lshlrev_b32_e32 v107, 4, v2
	v_bitop3_b32 v2, v98, v4, 6 bitop3:0x36
	v_lshl_or_b32 v3, v101, 14, v3
	v_lshlrev_b32_e32 v108, 4, v2
	v_mov_b32_e32 v66, 0
	v_mov_b32_e32 v2, 0
	v_lshlrev_b32_e32 v99, 3, v0
	v_add_u32_e32 v104, 0x16800, v3
	s_mov_b32 s7, 0
	s_mov_b32 s17, 0x55555556
	s_mov_b64 s[8:9], 0x6000
	s_mov_b64 s[10:11], 0x4000
	s_mov_b64 s[12:13], 0x2000
	s_mov_b32 s6, 0
	s_mov_b32 s18, 0
	s_mov_b32 s19, 0
	v_mov_b32_e32 v3, v2
	v_mov_b32_e32 v4, v2
	v_mov_b32_e32 v5, v2
	v_mov_b32_e32 v6, v2
	v_mov_b32_e32 v7, v2
	v_mov_b32_e32 v8, v2
	v_mov_b32_e32 v9, v2
	v_mov_b32_e32 v10, v2
	v_mov_b32_e32 v11, v2
	v_mov_b32_e32 v12, v2
	v_mov_b32_e32 v13, v2
	v_mov_b32_e32 v14, v2
	v_mov_b32_e32 v15, v2
	v_mov_b32_e32 v16, v2
	v_mov_b32_e32 v17, v2
	v_mov_b32_e32 v18, v2
	v_mov_b32_e32 v19, v2
	v_mov_b32_e32 v20, v2
	v_mov_b32_e32 v21, v2
	v_mov_b32_e32 v22, v2
	v_mov_b32_e32 v23, v2
	v_mov_b32_e32 v24, v2
	v_mov_b32_e32 v25, v2
	v_mov_b32_e32 v26, v2
	v_mov_b32_e32 v27, v2
	v_mov_b32_e32 v28, v2
	v_mov_b32_e32 v29, v2
	v_mov_b32_e32 v30, v2
	v_mov_b32_e32 v31, v2
	v_mov_b32_e32 v32, v2
	v_mov_b32_e32 v33, v2
	v_mov_b32_e32 v34, v2
	v_mov_b32_e32 v35, v2
	v_mov_b32_e32 v36, v2
	v_mov_b32_e32 v37, v2
	v_mov_b32_e32 v38, v2
	v_mov_b32_e32 v39, v2
	v_mov_b32_e32 v40, v2
	v_mov_b32_e32 v41, v2
	v_mov_b32_e32 v42, v2
	v_mov_b32_e32 v43, v2
	v_mov_b32_e32 v44, v2
	v_mov_b32_e32 v45, v2
	v_mov_b32_e32 v46, v2
	v_mov_b32_e32 v47, v2
	v_mov_b32_e32 v48, v2
	v_mov_b32_e32 v49, v2
	v_mov_b32_e32 v50, v2
	v_mov_b32_e32 v51, v2
	v_mov_b32_e32 v52, v2
	v_mov_b32_e32 v53, v2
	v_mov_b32_e32 v54, v2
	v_mov_b32_e32 v55, v2
	v_mov_b32_e32 v56, v2
	v_mov_b32_e32 v57, v2
	v_mov_b32_e32 v58, v2
	v_mov_b32_e32 v59, v2
	v_mov_b32_e32 v60, v2
	v_mov_b32_e32 v61, v2
	v_mov_b32_e32 v62, v2
	v_mov_b32_e32 v63, v2
	v_mov_b32_e32 v64, v2
	v_mov_b32_e32 v65, v2
	v_mov_b32_e32 v67, v66
	v_mov_b32_e32 v68, v66
	v_mov_b32_e32 v69, v66
	v_mov_b32_e32 v78, v66
	v_mov_b32_e32 v79, v66
	v_mov_b32_e32 v80, v66
	v_mov_b32_e32 v81, v66
	v_mov_b32_e32 v70, v66
	v_mov_b32_e32 v71, v66
	v_mov_b32_e32 v72, v66
	v_mov_b32_e32 v73, v66
	v_mov_b32_e32 v74, v66
	v_mov_b32_e32 v75, v66
	v_mov_b32_e32 v76, v66
	v_mov_b32_e32 v77, v66
	s_waitcnt vmcnt(0) lgkmcnt(0)
	s_barrier
	s_branch .LBB11_6

amdhsa.kernels:
  - .agpr_count:     0
    .args:
      - .offset:         0
        .size:           240
        .value_kind:     by_value
      - .actual_access:  write_only
        .address_space:  global
        .offset:         240
        .size:           8
        .value_kind:     global_buffer
      - .offset:         248
        .size:           4
        .value_kind:     hidden_block_count_x
      - .offset:         252
        .size:           4
        .value_kind:     hidden_block_count_y
      - .offset:         256
        .size:           4
        .value_kind:     hidden_block_count_z
      - .offset:         260
        .size:           2
        .value_kind:     hidden_group_size_x
      - .offset:         262
        .size:           2
        .value_kind:     hidden_group_size_y
      - .offset:         264
        .size:           2
        .value_kind:     hidden_group_size_z
      - .offset:         266
        .size:           2
        .value_kind:     hidden_remainder_x
      - .offset:         268
        .size:           2
        .value_kind:     hidden_remainder_y
      - .offset:         270
        .size:           2
        .value_kind:     hidden_remainder_z
      - .offset:         288
        .size:           8
        .value_kind:     hidden_global_offset_x
      - .offset:         296
        .size:           8
        .value_kind:     hidden_global_offset_y
      - .offset:         304
        .size:           8
        .value_kind:     hidden_global_offset_z
      - .offset:         312
        .size:           2
        .value_kind:     hidden_grid_dims
    .group_segment_fixed_size: 0
    .kernarg_segment_align: 8
    .kernarg_segment_size: 504
    .language:       OpenCL C
    .language_version:
      - 2
      - 0
    .max_flat_workgroup_size: 256
    .name:           _Z11prep_kernel8PrepArgsPc
    .private_segment_fixed_size: 0
    .sgpr_count:     50
    .sgpr_spill_count: 0
    .symbol:         _Z11prep_kernel8PrepArgsPc.kd
    .uniform_work_group_size: 1
    .uses_dynamic_stack: false
    .vgpr_count:     30
    .vgpr_spill_count: 0
    .wavefront_size: 64
  - .agpr_count:     16
    .args:
      - .actual_access:  read_only
        .address_space:  global
        .offset:         0
        .size:           8
        .value_kind:     global_buffer
      - .actual_access:  read_only
        .address_space:  global
        .offset:         8
        .size:           8
        .value_kind:     global_buffer
      - .actual_access:  read_only
        .address_space:  global
        .offset:         16
        .size:           8
        .value_kind:     global_buffer
      - .actual_access:  write_only
        .address_space:  global
        .offset:         24
        .size:           8
        .value_kind:     global_buffer
    .group_segment_fixed_size: 0
    .kernarg_segment_align: 8
    .kernarg_segment_size: 32
    .language:       OpenCL C
    .language_version:
      - 2
      - 0
    .max_flat_workgroup_size: 256
    .name:           _Z12conv1_kernelPKfPKDF16_S0_PDF16_
    .private_segment_fixed_size: 0
    .sgpr_count:     47
    .sgpr_spill_count: 0
    .symbol:         _Z12conv1_kernelPKfPKDF16_S0_PDF16_.kd
    .uniform_work_group_size: 1
    .uses_dynamic_stack: false
    .vgpr_count:     116
    .vgpr_spill_count: 0
    .wavefront_size: 64
  - .agpr_count:     32
    .args:
      - .actual_access:  read_only
        .address_space:  global
        .offset:         0
        .size:           8
        .value_kind:     global_buffer
      - .actual_access:  read_only
        .address_space:  global
        .offset:         8
        .size:           8
        .value_kind:     global_buffer
      - .actual_access:  read_only
        .address_space:  global
        .offset:         16
        .size:           8
        .value_kind:     global_buffer
      - .actual_access:  write_only
        .address_space:  global
        .offset:         24
        .size:           8
        .value_kind:     global_buffer
      - .actual_access:  write_only
        .address_space:  global
        .offset:         32
        .size:           8
        .value_kind:     global_buffer
    .group_segment_fixed_size: 0
    .kernarg_segment_align: 8
    .kernarg_segment_size: 40
    .language:       OpenCL C
    .language_version:
      - 2
      - 0
    .max_flat_workgroup_size: 64
    .name:           _Z11gat1_kernelPKDF16_S0_PKfPDF16_Pf
    .private_segment_fixed_size: 0
    .sgpr_count:     20
    .sgpr_spill_count: 0
    .symbol:         _Z11gat1_kernelPKDF16_S0_PKfPDF16_Pf.kd
    .uniform_work_group_size: 1
    .uses_dynamic_stack: false
    .vgpr_count:     284
    .vgpr_spill_count: 0
    .wavefront_size: 64
  - .agpr_count:     32
    .args:
      - .actual_access:  read_only
        .address_space:  global
        .offset:         0
        .size:           8
        .value_kind:     global_buffer
      - .actual_access:  read_only
        .address_space:  global
        .offset:         8
        .size:           8
        .value_kind:     global_buffer
      - .actual_access:  read_only
        .address_space:  global
        .offset:         16
        .size:           8
        .value_kind:     global_buffer
      - .actual_access:  read_only
        .address_space:  global
        .offset:         24
        .size:           8
        .value_kind:     global_buffer
      - .actual_access:  read_only
        .address_space:  global
        .offset:         32
        .size:           8
        .value_kind:     global_buffer
      - .actual_access:  write_only
        .address_space:  global
        .offset:         40
        .size:           8
        .value_kind:     global_buffer
      - .actual_access:  write_only
        .address_space:  global
        .offset:         48
        .size:           8
        .value_kind:     global_buffer
      - .actual_access:  read_only
        .address_space:  global
        .offset:         56
        .size:           8
        .value_kind:     global_buffer
      - .actual_access:  read_only
        .address_space:  global
        .offset:         64
        .size:           8
        .value_kind:     global_buffer
      - .actual_access:  read_only
        .address_space:  global
        .offset:         72
        .size:           8
        .value_kind:     global_buffer
      - .address_space:  global
        .offset:         80
        .size:           8
        .value_kind:     global_buffer
    .group_segment_fixed_size: 36880
    .kernarg_segment_align: 8
    .kernarg_segment_size: 88
    .language:       OpenCL C
    .language_version:
      - 2
      - 0
    .max_flat_workgroup_size: 256
    .name:           _Z11gat2_kernelPKfPKDF16_S0_S2_S0_PDF16_PfS2_S2_S0_S4_
    .private_segment_fixed_size: 0
    .sgpr_count:     22
    .sgpr_spill_count: 0
    .symbol:         _Z11gat2_kernelPKfPKDF16_S0_S2_S0_PDF16_PfS2_S2_S0_S4_.kd
    .uniform_work_group_size: 1
    .uses_dynamic_stack: false
    .vgpr_count:     264
    .vgpr_spill_count: 0
    .wavefront_size: 64
  - .agpr_count:     16
    .args:
      - .actual_access:  read_only
        .address_space:  global
        .offset:         0
        .size:           8
        .value_kind:     global_buffer
      - .actual_access:  read_only
        .address_space:  global
        .offset:         8
        .size:           8
        .value_kind:     global_buffer
      - .actual_access:  read_only
        .address_space:  global
        .offset:         16
        .size:           8
        .value_kind:     global_buffer
      - .address_space:  global
        .offset:         24
        .size:           8
        .value_kind:     global_buffer
    .group_segment_fixed_size: 1040
    .kernarg_segment_align: 8
    .kernarg_segment_size: 32
    .language:       OpenCL C
    .language_version:
      - 2
      - 0
    .max_flat_workgroup_size: 256
    .name:           _Z11gat3_kernelPKfPKDF16_S0_Pf
    .private_segment_fixed_size: 0
    .sgpr_count:     18
    .sgpr_spill_count: 0
    .symbol:         _Z11gat3_kernelPKfPKDF16_S0_Pf.kd
    .uniform_work_group_size: 1
    .uses_dynamic_stack: false
    .vgpr_count:     192
    .vgpr_spill_count: 0
    .wavefront_size: 64
  - .agpr_count:     0
    .args:
      - .actual_access:  read_only
        .address_space:  global
        .offset:         0
        .size:           8
        .value_kind:     global_buffer
      - .actual_access:  read_only
        .address_space:  global
        .offset:         8
        .size:           8
        .value_kind:     global_buffer
      - .actual_access:  read_only
        .address_space:  global
        .offset:         16
        .size:           8
        .value_kind:     global_buffer
      - .actual_access:  read_only
        .address_space:  global
        .offset:         24
        .size:           8
        .value_kind:     global_buffer
      - .actual_access:  read_only
        .address_space:  global
        .offset:         32
        .size:           8
        .value_kind:     global_buffer
      - .actual_access:  read_only
        .address_space:  global
        .offset:         40
        .size:           8
        .value_kind:     global_buffer
      - .actual_access:  write_only
        .address_space:  global
        .offset:         48
        .size:           8
        .value_kind:     global_buffer
    .group_segment_fixed_size: 87680
    .kernarg_segment_align: 8
    .kernarg_segment_size: 56
    .language:       OpenCL C
    .language_version:
      - 2
      - 0
    .max_flat_workgroup_size: 512
    .name:           _Z12gat3p_kernelPKfPKDF16_S0_S0_S0_S0_Pf
    .private_segment_fixed_size: 0
    .sgpr_count:     78
    .sgpr_spill_count: 0
    .symbol:         _Z12gat3p_kernelPKfPKDF16_S0_S0_S0_S0_Pf.kd
    .uniform_work_group_size: 1
    .uses_dynamic_stack: false
    .vgpr_count:     206
    .vgpr_spill_count: 0
    .wavefront_size: 64
  - .agpr_count:     0
    .args:
      - .actual_access:  read_only
        .address_space:  global
        .offset:         0
        .size:           8
        .value_kind:     global_buffer
      - .actual_access:  read_only
        .address_space:  global
        .offset:         8
        .size:           8
        .value_kind:     global_buffer
      - .actual_access:  read_only
        .address_space:  global
        .offset:         16
        .size:           8
        .value_kind:     global_buffer
      - .address_space:  global
        .offset:         24
        .size:           8
        .value_kind:     global_buffer
    .group_segment_fixed_size: 2048
    .kernarg_segment_align: 8
    .kernarg_segment_size: 32
    .language:       OpenCL C
    .language_version:
      - 2
      - 0
    .max_flat_workgroup_size: 64
    .name:           _Z12gat3s_kernelPKfPKDF16_S0_Pf
    .private_segment_fixed_size: 0
    .sgpr_count:     26
    .sgpr_spill_count: 0
    .symbol:         _Z12gat3s_kernelPKfPKDF16_S0_Pf.kd
    .uniform_work_group_size: 1
    .uses_dynamic_stack: false
    .vgpr_count:     192
    .vgpr_spill_count: 0
    .wavefront_size: 64
  - .agpr_count:     0
    .args:
      - .actual_access:  read_only
        .address_space:  global
        .offset:         0
        .size:           8
        .value_kind:     global_buffer
      - .actual_access:  read_only
        .address_space:  global
        .offset:         8
        .size:           8
        .value_kind:     global_buffer
      - .actual_access:  read_only
        .address_space:  global
        .offset:         16
        .size:           8
        .value_kind:     global_buffer
      - .actual_access:  write_only
        .address_space:  global
        .offset:         24
        .size:           8
        .value_kind:     global_buffer
    .group_segment_fixed_size: 13952
    .kernarg_segment_align: 8
    .kernarg_segment_size: 32
    .language:       OpenCL C
    .language_version:
      - 2
      - 0
    .max_flat_workgroup_size: 256
    .name:           _Z11head_kernelPKfS0_S0_Pf
    .private_segment_fixed_size: 0
    .sgpr_count:     15
    .sgpr_spill_count: 0
    .symbol:         _Z11head_kernelPKfS0_S0_Pf.kd
    .uniform_work_group_size: 1
    .uses_dynamic_stack: false
    .vgpr_count:     38
    .vgpr_spill_count: 0
    .wavefront_size: 64
  - .agpr_count:     0
    .args:
      - .actual_access:  read_only
        .address_space:  global
        .offset:         0
        .size:           8
        .value_kind:     global_buffer
      - .actual_access:  read_only
        .address_space:  global
        .offset:         8
        .size:           8
        .value_kind:     global_buffer
      - .actual_access:  read_only
        .address_space:  global
        .offset:         16
        .size:           8
        .value_kind:     global_buffer
      - .actual_access:  write_only
        .address_space:  global
        .offset:         24
        .size:           8
        .value_kind:     global_buffer
    .group_segment_fixed_size: 640
    .kernarg_segment_align: 8
    .kernarg_segment_size: 32
    .language:       OpenCL C
    .language_version:
      - 2
      - 0
    .max_flat_workgroup_size: 256
    .name:           _Z12final_kernelPKfS0_S0_Pf
    .private_segment_fixed_size: 0
    .sgpr_count:     18
    .sgpr_spill_count: 0
    .symbol:         _Z12final_kernelPKfS0_S0_Pf.kd
    .uniform_work_group_size: 1
    .uses_dynamic_stack: false
    .vgpr_count:     37
    .vgpr_spill_count: 0
    .wavefront_size: 64
  - .agpr_count:     0
    .args:
      - .actual_access:  read_only
        .address_space:  global
        .offset:         0
        .size:           8
        .value_kind:     global_buffer
      - .address_space:  global
        .offset:         8
        .size:           8
        .value_kind:     global_buffer
      - .actual_access:  read_only
        .address_space:  global
        .offset:         16
        .size:           8
        .value_kind:     global_buffer
      - .actual_access:  write_only
        .address_space:  global
        .offset:         24
        .size:           8
        .value_kind:     global_buffer
      - .actual_access:  read_only
        .address_space:  global
        .offset:         32
        .size:           8
        .value_kind:     global_buffer
      - .actual_access:  read_only
        .address_space:  global
        .offset:         40
        .size:           8
        .value_kind:     global_buffer
      - .actual_access:  read_only
        .address_space:  global
        .offset:         48
        .size:           8
        .value_kind:     global_buffer
      - .actual_access:  read_only
        .address_space:  global
        .offset:         56
        .size:           8
        .value_kind:     global_buffer
      - .offset:         64
        .size:           4
        .value_kind:     hidden_block_count_x
      - .offset:         68
        .size:           4
        .value_kind:     hidden_block_count_y
      - .offset:         72
        .size:           4
        .value_kind:     hidden_block_count_z
      - .offset:         76
        .size:           2
        .value_kind:     hidden_group_size_x
      - .offset:         78
        .size:           2
        .value_kind:     hidden_group_size_y
      - .offset:         80
        .size:           2
        .value_kind:     hidden_group_size_z
      - .offset:         82
        .size:           2
        .value_kind:     hidden_remainder_x
      - .offset:         84
        .size:           2
        .value_kind:     hidden_remainder_y
      - .offset:         86
        .size:           2
        .value_kind:     hidden_remainder_z
      - .offset:         104
        .size:           8
        .value_kind:     hidden_global_offset_x
      - .offset:         112
        .size:           8
        .value_kind:     hidden_global_offset_y
      - .offset:         120
        .size:           8
        .value_kind:     hidden_global_offset_z
      - .offset:         128
        .size:           2
        .value_kind:     hidden_grid_dims
    .group_segment_fixed_size: 74240
    .kernarg_segment_align: 8
    .kernarg_segment_size: 320
    .language:       OpenCL C
    .language_version:
      - 2
      - 0
    .max_flat_workgroup_size: 256
    .name:           _Z11conv_kernelILi64ELi128ELi128ELi128ELi4ELi2ELi2ELb1ELi1ELb0ELb0ELi2EEvPKDF16_S1_PKfPDF16_S1_S3_S1_S3_
    .private_segment_fixed_size: 0
    .sgpr_count:     58
    .sgpr_spill_count: 0
    .symbol:         _Z11conv_kernelILi64ELi128ELi128ELi128ELi4ELi2ELi2ELb1ELi1ELb0ELb0ELi2EEvPKDF16_S1_PKfPDF16_S1_S3_S1_S3_.kd
    .uniform_work_group_size: 1
    .uses_dynamic_stack: false
    .vgpr_count:     256
    .vgpr_spill_count: 0
    .wavefront_size: 64
  - .agpr_count:     0
    .args:
      - .address_space:  global
        .offset:         0
        .size:           8
        .value_kind:     global_buffer
      - .address_space:  global
        .offset:         8
        .size:           8
        .value_kind:     global_buffer
      - .actual_access:  read_only
        .address_space:  global
        .offset:         16
        .size:           8
        .value_kind:     global_buffer
      - .actual_access:  write_only
        .address_space:  global
        .offset:         24
        .size:           8
        .value_kind:     global_buffer
      - .address_space:  global
        .offset:         32
        .size:           8
        .value_kind:     global_buffer
      - .actual_access:  read_only
        .address_space:  global
        .offset:         40
        .size:           8
        .value_kind:     global_buffer
      - .actual_access:  read_only
        .address_space:  global
        .offset:         48
        .size:           8
        .value_kind:     global_buffer
      - .actual_access:  read_only
        .address_space:  global
        .offset:         56
        .size:           8
        .value_kind:     global_buffer
      - .offset:         64
        .size:           4
        .value_kind:     hidden_block_count_x
      - .offset:         68
        .size:           4
        .value_kind:     hidden_block_count_y
      - .offset:         72
        .size:           4
        .value_kind:     hidden_block_count_z
      - .offset:         76
        .size:           2
        .value_kind:     hidden_group_size_x
      - .offset:         78
        .size:           2
        .value_kind:     hidden_group_size_y
      - .offset:         80
        .size:           2
        .value_kind:     hidden_group_size_z
      - .offset:         82
        .size:           2
        .value_kind:     hidden_remainder_x
      - .offset:         84
        .size:           2
        .value_kind:     hidden_remainder_y
      - .offset:         86
        .size:           2
        .value_kind:     hidden_remainder_z
      - .offset:         104
        .size:           8
        .value_kind:     hidden_global_offset_x
      - .offset:         112
        .size:           8
        .value_kind:     hidden_global_offset_y
      - .offset:         120
        .size:           8
        .value_kind:     hidden_global_offset_z
      - .offset:         128
        .size:           2
        .value_kind:     hidden_grid_dims
    .group_segment_fixed_size: 148480
    .kernarg_segment_align: 8
    .kernarg_segment_size: 320
    .language:       OpenCL C
    .language_version:
      - 2
      - 0
    .max_flat_workgroup_size: 512
    .name:           _Z11conv_kernelILi128ELi256ELi64ELi64ELi4ELi2ELi4ELb0ELi1ELb1ELb0ELi1EEvPKDF16_S1_PKfPDF16_S1_S3_S1_S3_
    .private_segment_fixed_size: 0
    .sgpr_count:     28
    .sgpr_spill_count: 0
    .symbol:         _Z11conv_kernelILi128ELi256ELi64ELi64ELi4ELi2ELi4ELb0ELi1ELb1ELb0ELi1EEvPKDF16_S1_PKfPDF16_S1_S3_S1_S3_.kd
    .uniform_work_group_size: 1
    .uses_dynamic_stack: false
    .vgpr_count:     234
    .vgpr_spill_count: 0
    .wavefront_size: 64
  - .agpr_count:     0
    .args:
      - .address_space:  global
        .offset:         0
        .size:           8
        .value_kind:     global_buffer
      - .address_space:  global
        .offset:         8
        .size:           8
        .value_kind:     global_buffer
      - .actual_access:  read_only
        .address_space:  global
        .offset:         16
        .size:           8
        .value_kind:     global_buffer
      - .actual_access:  write_only
        .address_space:  global
        .offset:         24
        .size:           8
        .value_kind:     global_buffer
      - .address_space:  global
        .offset:         32
        .size:           8
        .value_kind:     global_buffer
      - .actual_access:  read_only
        .address_space:  global
        .offset:         40
        .size:           8
        .value_kind:     global_buffer
      - .actual_access:  read_only
        .address_space:  global
        .offset:         48
        .size:           8
        .value_kind:     global_buffer
      - .actual_access:  read_only
        .address_space:  global
        .offset:         56
        .size:           8
        .value_kind:     global_buffer
      - .offset:         64
        .size:           4
        .value_kind:     hidden_block_count_x
      - .offset:         68
        .size:           4
        .value_kind:     hidden_block_count_y
      - .offset:         72
        .size:           4
        .value_kind:     hidden_block_count_z
      - .offset:         76
        .size:           2
        .value_kind:     hidden_group_size_x
      - .offset:         78
        .size:           2
        .value_kind:     hidden_group_size_y
      - .offset:         80
        .size:           2
        .value_kind:     hidden_group_size_z
      - .offset:         82
        .size:           2
        .value_kind:     hidden_remainder_x
      - .offset:         84
        .size:           2
        .value_kind:     hidden_remainder_y
      - .offset:         86
        .size:           2
        .value_kind:     hidden_remainder_z
      - .offset:         104
        .size:           8
        .value_kind:     hidden_global_offset_x
      - .offset:         112
        .size:           8
        .value_kind:     hidden_global_offset_y
      - .offset:         120
        .size:           8
        .value_kind:     hidden_global_offset_z
      - .offset:         128
        .size:           2
        .value_kind:     hidden_grid_dims
    .group_segment_fixed_size: 157696
    .kernarg_segment_align: 8
    .kernarg_segment_size: 320
    .language:       OpenCL C
    .language_version:
      - 2
      - 0
    .max_flat_workgroup_size: 512
    .name:           _Z11conv_kernelILi256ELi256ELi32ELi32ELi2ELi2ELi2ELb0ELi2ELb0ELb1ELi1EEvPKDF16_S1_PKfPDF16_S1_S3_S1_S3_
    .private_segment_fixed_size: 0
    .sgpr_count:     30
    .sgpr_spill_count: 0
    .symbol:         _Z11conv_kernelILi256ELi256ELi32ELi32ELi2ELi2ELi2ELb0ELi2ELb0ELb1ELi1EEvPKDF16_S1_PKfPDF16_S1_S3_S1_S3_.kd
    .uniform_work_group_size: 1
    .uses_dynamic_stack: false
    .vgpr_count:     121
    .vgpr_spill_count: 0
    .wavefront_size: 64
